# v23: v21 + attention tile loop: next K/V tile staged global->LDS by LDS-DMA (K at half-step start, V after the post-pv barrier) instead of 16 staging VGPRs + ds_write
# speedup vs baseline: 1.0089x; 1.0089x over previous
; __device__ __forceinline__ int v_st(int k, int c) { const int kk = (k & ~0xC) | ((k & 4) << 1) | ((k & 8) >> 1); return ((kk >> 3) * 4 + (c >> 5)) * 512 + ((kk & 7) * 32 + (c & 31)) * 2; }
; __device__ __forceinline__ int v_rd_base(int lane) { return ((lane & 3) << 3) | (((lane >> 2) & 3) << 6) | (((lane >> 4) & 1) << 5) | (((lane >> 5) & 1) << 8); }
; template <class TIn, class TOut, int QS, int KS, int OS, bool BIAS, bool PREF = true>
; __device__ __forceinline__ void causal_swa_block(const BlockRef<TIn, TOut>& cur, const BlockRef<TIn, TOut>& nxt, int skv, int W, char* lds, Seam<TIn>& S) {
;     ...
;     float m_reg = BIAS ? ((const float*)(lds + BIAS_OFF))[cur.P0 + wid * QBLK + r32] : -1e30f, l_reg = 0; f32x16 o[4] = {};
;     const int sr = tid >> 4, sc = (tid & 15) * 8, vst0 = v_st(sr, sc), vst1 = v_st(32 + sr, sc), kws = KSWZ(sr, sc * 2);
;     const int vb0 = (int)(uintptr_t)V_lds + v_rd_base(lane);
;     const TIn* Kh = cur.K; const TIn* Vh = cur.V;
;     const float* bias0 = (const float*)(lds + BIAS_OFF) + 4 * hi;
.LBB0_471:
	v_exp_f32_e32 v176, v21
	v_sub_f32_e32 v21, v54, v55
	v_mul_f32_e32 v21, 0x3e0293ee, v21
	v_exp_f32_e32 v21, v21
	v_exp_f32_e32 v175, v56
	v_exp_f32_e32 v177, v57
	v_exp_f32_e32 v173, v58
	v_cndmask_b32_e64 v223, v21, 1.0, s[0:1]
	s_and_b32 s0, s21, 0x3fffffc0
	s_lshl_b32 s0, s0, 2
	s_add_i32 s0, s0, 0
	v_exp_f32_e32 v172, v22
	v_exp_f32_e32 v174, v23
	v_exp_f32_e32 v170, v24
	v_exp_f32_e32 v171, v25
	v_exp_f32_e32 v165, v26
	v_exp_f32_e32 v168, v27
	v_exp_f32_e32 v163, v28
	v_exp_f32_e32 v166, v29
	v_exp_f32_e32 v162, v30
	v_exp_f32_e32 v169, v18
	v_exp_f32_e32 v164, v19
	v_exp_f32_e32 v167, v20
	v_pk_fma_f32 v[128:129], v[2:3], s[20:21], v[52:53] op_sel_hi:[1,0,0]
	s_add_i32 s0, s0, 0x10000
	v_lshlrev_b32_e32 v3, 1, v0
	v_pk_fma_f32 v[126:127], v[4:5], s[20:21], v[52:53] op_sel_hi:[1,0,0]
	v_and_b32_e32 v2, 0xc0, v50
	v_and_b32_e32 v3, 32, v3
	v_and_b32_e32 v4, 0x118, v53
	s_cmp_lg_u32 0, -1
	v_or3_b32 v2, v3, v2, v4
	s_cselect_b32 s1, 0, 0
	v_pk_fma_f32 v[114:115], v[16:17], s[20:21], v[52:53] op_sel_hi:[1,0,0]
	v_pk_fma_f32 v[116:117], v[14:15], s[20:21], v[52:53] op_sel_hi:[1,0,0]
	v_pk_fma_f32 v[118:119], v[12:13], s[20:21], v[52:53] op_sel_hi:[1,0,0]
	v_pk_fma_f32 v[120:121], v[10:11], s[20:21], v[52:53] op_sel_hi:[1,0,0]
	v_pk_fma_f32 v[122:123], v[8:9], s[20:21], v[52:53] op_sel_hi:[1,0,0]
	v_pk_fma_f32 v[124:125], v[6:7], s[20:21], v[52:53] op_sel_hi:[1,0,0]
	s_mov_b32 s35, 2
	v_add_u32_e32 v199, s1, v2
	s_cmp_lt_i32 s34, 3
	v_lshl_add_u32 v220, v216, 2, s0
	v_lshl_add_u32 v219, v217, 2, s0
	s_waitcnt lgkmcnt(0)
	s_barrier
	s_cbranch_scc1 .LBB0_492
	v_add_u32_e32 v2, s15, v216
	v_subrev_u32_e32 v2, s4, v2
	s_lshl_b32 s0, s4, 2
	v_sub_u32_e32 v2, v2, v217
	s_add_i32 s36, s4, 0x7f
	s_add_i32 s0, s0, 0
	v_add_u32_e32 v225, 0xffffff45, v2
	v_add_u32_e32 v2, s0, v196
	s_add_u32 s0, s6, s18
	s_addc_u32 s1, s7, s19
	s_add_u32 s0, s0, s10
	s_addc_u32 s1, s1, s11
	v_add_u32_e32 v226, 0x10900, v2
	v_mov_b32_e32 v195, 0
	v_lshrrev_b32_e32 v254, 2, v0
	v_and_b32_e32 v254, 7, v254
	v_lshrrev_b32_e32 v255, 7, v0
	v_lshl_or_b32 v254, v255, 3, v254
	v_and_b32_e32 v253, 4, v254
	v_lshlrev_b32_e32 v253, 1, v253
	v_and_b32_e32 v255, 8, v254
	v_lshrrev_b32_e32 v255, 1, v255
	v_or_b32_e32 v253, v253, v255
	v_and_b32_e32 v254, 0x13, v254
	v_or_b32_e32 v254, v254, v253
	v_lshlrev_b32_e32 v254, 11, v254
	v_lshrrev_b32_e32 v253, 5, v0
	v_and_b32_e32 v253, 3, v253
	v_lshlrev_b32_e32 v253, 6, v253
	v_and_b32_e32 v255, 3, v0
	v_lshlrev_b32_e32 v255, 4, v255
	v_or3_b32 v254, v254, v253, v255
	v_lshrrev_b32_e32 v253, 4, v0
	v_and_b32_e32 v253, 7, v253
	v_lshlrev_b32_e32 v253, 4, v253
	v_xor_b32_e32 v253, v253, v194
	s_add_u32 s0, s72, s0
	v_add_u32_e32 v2, v51, v197
	v_mov_b32_e32 v3, 0x10000
	v_cmp_gt_u32_e64 s[2:3], 32, v198
	s_addc_u32 s1, s73, s1
	v_lshl_add_u32 v202, v2, 1, v3
	v_mov_b32_e32 v203, v195
	s_mov_b32 s19, 0x9640000
	s_mov_b32 s37, 0x7640000
	s_mov_b32 s38, 0x41000000
	s_mov_b32 s18, 0x3e0293ee
	v_mov_b32_e32 v227, 0xff800000
	v_mov_b32_e32 v224, v195
	v_mov_b32_e32 v50, v195
	v_mov_b32_e32 v51, v195
	v_mov_b32_e32 v52, v195
	v_mov_b32_e32 v53, v195
	v_mov_b32_e32 v54, v195
	v_mov_b32_e32 v55, v195
	v_mov_b32_e32 v56, v195
	v_mov_b32_e32 v57, v195
	v_mov_b32_e32 v58, v195
	v_mov_b32_e32 v59, v195
	v_mov_b32_e32 v60, v195
	v_mov_b32_e32 v61, v195
	v_mov_b32_e32 v62, v195
	v_mov_b32_e32 v63, v195
	v_mov_b32_e32 v64, v195
	v_mov_b32_e32 v65, v195
	v_mov_b32_e32 v34, v195
	v_mov_b32_e32 v35, v195
	v_mov_b32_e32 v36, v195
	v_mov_b32_e32 v37, v195
	v_mov_b32_e32 v38, v195
	v_mov_b32_e32 v39, v195
	v_mov_b32_e32 v40, v195
	v_mov_b32_e32 v41, v195
	v_mov_b32_e32 v42, v195
	v_mov_b32_e32 v43, v195
	v_mov_b32_e32 v44, v195
	v_mov_b32_e32 v45, v195
	v_mov_b32_e32 v46, v195
	v_mov_b32_e32 v47, v195
	v_mov_b32_e32 v48, v195
	v_mov_b32_e32 v49, v195
	v_mov_b32_e32 v18, v195
	v_mov_b32_e32 v19, v195
	v_mov_b32_e32 v20, v195
	v_mov_b32_e32 v21, v195
	v_mov_b32_e32 v22, v195
	v_mov_b32_e32 v23, v195
	v_mov_b32_e32 v24, v195
	v_mov_b32_e32 v25, v195
	v_mov_b32_e32 v26, v195
	v_mov_b32_e32 v27, v195
	v_mov_b32_e32 v28, v195
	v_mov_b32_e32 v29, v195
	v_mov_b32_e32 v30, v195
	v_mov_b32_e32 v31, v195
	v_mov_b32_e32 v32, v195
	v_mov_b32_e32 v33, v195
	v_mov_b32_e32 v2, v195
	v_mov_b32_e32 v3, v195
	v_mov_b32_e32 v4, v195
	v_mov_b32_e32 v5, v195
	v_mov_b32_e32 v6, v195
	v_mov_b32_e32 v7, v195
	v_mov_b32_e32 v8, v195
	v_mov_b32_e32 v9, v195
	v_mov_b32_e32 v10, v195
	v_mov_b32_e32 v11, v195
	v_mov_b32_e32 v12, v195
	v_mov_b32_e32 v13, v195
	v_mov_b32_e32 v14, v195
	v_mov_b32_e32 v15, v195
	v_mov_b32_e32 v16, v195
	v_mov_b32_e32 v17, v195
	s_branch .LBB0_475
.LBB0_473:
	s_or_b64 exec, exec, s[20:21]
	s_waitcnt lgkmcnt(0)
	ds_read_b128 v[164:167], v219 offset:224
	ds_read_b128 v[168:171], v219 offset:192
	ds_read_b128 v[172:175], v219 offset:160
	ds_read_b128 v[180:183], v219 offset:128
	s_waitcnt lgkmcnt(3)
	v_pk_mul_f32 v[64:65], v[64:65], v[166:167]
	s_waitcnt lgkmcnt(2)
	v_pk_mul_f32 v[60:61], v[60:61], v[170:171]
	s_waitcnt lgkmcnt(1)
	v_pk_mul_f32 v[56:57], v[56:57], v[174:175]
	s_waitcnt lgkmcnt(0)
	v_pk_mul_f32 v[52:53], v[52:53], v[182:183]
	v_pk_mul_f32 v[62:63], v[62:63], v[164:165]
	v_pk_mul_f32 v[58:59], v[58:59], v[168:169]
	v_pk_mul_f32 v[54:55], v[54:55], v[172:173]
	v_pk_mul_f32 v[50:51], v[50:51], v[180:181]
	v_pk_mul_f32 v[48:49], v[48:49], v[166:167]
	v_pk_mul_f32 v[44:45], v[44:45], v[170:171]
	v_pk_mul_f32 v[40:41], v[40:41], v[174:175]
	v_pk_mul_f32 v[36:37], v[36:37], v[182:183]
	v_pk_mul_f32 v[46:47], v[46:47], v[164:165]
	v_pk_mul_f32 v[42:43], v[42:43], v[168:169]
	v_pk_mul_f32 v[38:39], v[38:39], v[172:173]
	v_pk_mul_f32 v[34:35], v[34:35], v[180:181]
	v_pk_mul_f32 v[32:33], v[32:33], v[166:167]
	v_pk_mul_f32 v[28:29], v[28:29], v[170:171]
	v_pk_mul_f32 v[24:25], v[24:25], v[174:175]
	v_pk_mul_f32 v[20:21], v[20:21], v[182:183]
	v_pk_mul_f32 v[30:31], v[30:31], v[164:165]
	v_pk_mul_f32 v[26:27], v[26:27], v[168:169]
	v_pk_mul_f32 v[22:23], v[22:23], v[172:173]
	v_pk_mul_f32 v[18:19], v[18:19], v[180:181]
	v_pk_mul_f32 v[16:17], v[16:17], v[166:167]
	v_pk_mul_f32 v[12:13], v[12:13], v[170:171]
	v_pk_mul_f32 v[8:9], v[8:9], v[174:175]
	v_pk_mul_f32 v[4:5], v[4:5], v[182:183]
	v_pk_mul_f32 v[14:15], v[14:15], v[164:165]
	v_pk_mul_f32 v[10:11], v[10:11], v[168:169]
	v_pk_mul_f32 v[6:7], v[6:7], v[172:173]
	v_pk_mul_f32 v[2:3], v[2:3], v[180:181]
; template <int KB, bool SK, bool BIAS>
; __device__ __forceinline__ void qkt(f32x16& p0, f32x16& p1, const char* K_lds, int r32, int hi, const bf16x8* qr, bool act, const float* bl) {
;     ...
;     const char* kb[4];
; #pragma unroll
;     for (int dd = 0; dd < 4; ++dd) kb[dd] = K_lds + KB * SHM_K + KSWZ(r32, (dd * 16 + hi * 8) * 2);
; #pragma unroll
;     for (int d0 = 0; d0 < 8; ++d0) { const char* a = kb[d0 & 3] + (d0 >> 2) * 128;
;         bf16x8 b0 = *reinterpret_cast<const bf16x8*>(a);
;         bf16x8 b1 = *reinterpret_cast<const bf16x8*>(a + 32 * 256);
;         p0 = __builtin_amdgcn_mfma_f32_32x32x16_bf16(b0, qr[d0], p0, 0, 0, 0);
;         p1 = __builtin_amdgcn_mfma_f32_32x32x16_bf16(b1, qr[d0], p1, 0, 0, 0); }
.LBB0_474:
	v_cndmask_b32_e64 v178, v162, v231, s[4:5]
	v_mul_f32_e32 v180, 0xbe0293ee, v178
	v_mov_b32_e32 v183, v180
	v_fmamk_f32 v162, v114, 0x3e0293ee, v180
	v_fmamk_f32 v163, v115, 0x3e0293ee, v180
	v_fmamk_f32 v164, v116, 0x3e0293ee, v180
	v_fmamk_f32 v165, v117, 0x3e0293ee, v180
	v_fmamk_f32 v166, v118, 0x3e0293ee, v180
	v_fmamk_f32 v167, v119, 0x3e0293ee, v180
	v_fmamk_f32 v168, v120, 0x3e0293ee, v180
	v_fmamk_f32 v169, v121, 0x3e0293ee, v180
	v_fmamk_f32 v181, v122, 0x3e0293ee, v180
	v_fmamk_f32 v182, v123, 0x3e0293ee, v180
	v_fmamk_f32 v124, v124, 0x3e0293ee, v180
	v_fmamk_f32 v125, v125, 0x3e0293ee, v180
	v_fmamk_f32 v126, v126, 0x3e0293ee, v180
	v_fmamk_f32 v127, v127, 0x3e0293ee, v180
	v_fmamk_f32 v128, v128, 0x3e0293ee, v180
	v_fmac_f32_e32 v183, 0x3e0293ee, v129
	v_exp_f32_e32 v175, v162
	v_exp_f32_e32 v177, v163
	v_exp_f32_e32 v173, v164
	v_exp_f32_e32 v176, v165
	v_exp_f32_e32 v172, v166
	v_exp_f32_e32 v174, v167
	v_exp_f32_e32 v170, v168
	v_exp_f32_e32 v171, v169
	v_exp_f32_e32 v165, v181
	v_exp_f32_e32 v168, v182
	v_exp_f32_e32 v163, v124
	v_exp_f32_e32 v166, v125
	v_exp_f32_e32 v162, v126
	v_exp_f32_e32 v169, v127
	v_exp_f32_e32 v164, v128
	v_exp_f32_e32 v167, v183
	s_addk_i32 s36, 0x80
	v_pk_fma_f32 v[128:129], v[98:99], s[18:19], v[180:181] op_sel_hi:[1,0,0]
	v_add_f32_e32 v98, v228, v229
	s_add_u32 s0, s0, 0x40000
	v_fmac_f32_e32 v98, v223, v224
	v_add_f32_e32 v224, v232, v233
	s_addc_u32 s1, s1, 0
	s_add_i32 s35, s35, 2
	v_pk_fma_f32 v[114:115], v[112:113], s[18:19], v[180:181] op_sel_hi:[1,0,0]
	v_pk_fma_f32 v[116:117], v[110:111], s[18:19], v[180:181] op_sel_hi:[1,0,0]
	v_pk_fma_f32 v[118:119], v[108:109], s[18:19], v[180:181] op_sel_hi:[1,0,0]
	v_pk_fma_f32 v[120:121], v[106:107], s[18:19], v[180:181] op_sel_hi:[1,0,0]
	v_pk_fma_f32 v[122:123], v[104:105], s[18:19], v[180:181] op_sel_hi:[1,0,0]
	v_pk_fma_f32 v[124:125], v[102:103], s[18:19], v[180:181] op_sel_hi:[1,0,0]
	v_pk_fma_f32 v[126:127], v[100:101], s[18:19], v[180:181] op_sel_hi:[1,0,0]
	v_fmac_f32_e32 v224, v98, v230
	v_add_u32_e32 v225, 0xffffff80, v225
	s_cmp_ge_i32 s35, s34
	v_add_u32_e32 v226, 0x200, v226
	v_mov_b32_e32 v223, v179
	s_waitcnt lgkmcnt(0)
	s_barrier
	s_cbranch_scc1 .LBB0_493
.LBB0_475:
	s_add_u32 s98, s0, 0x7640000
	s_addc_u32 s99, s1, 0
	s_lshl_b32 s100, s75, 10
	s_add_i32 m0, s100, 0x8000
	s_nop 0
	global_load_lds_dwordx4 v253, s[98:99]
	s_add_u32 s98, s98, 0x10000
	s_addc_u32 s99, s99, 0
	s_add_i32 m0, m0, 0x2000
	s_nop 0
	global_load_lds_dwordx4 v253, s[98:99]
	ds_read_b128 v[66:69], v208 offset:49152
	ds_read_b128 v[86:89], v226
	ds_read_b128 v[90:93], v226 offset:32
	ds_read_b128 v[94:97], v226 offset:64
	ds_read_b128 v[98:101], v226 offset:96
	ds_read_b128 v[102:105], v208 offset:57344
	ds_read_b128 v[106:109], v208 offset:49280
	v_add_f32_e32 v179, 0, v175
	v_add_f32_e32 v179, v177, v179
	s_waitcnt lgkmcnt(2)
	v_mfma_f32_32x32x16_bf16 v[86:101], v[66:69], v[158:161], v[86:101]
	ds_read_b128 v[70:73], v226 offset:128
	ds_read_b128 v[74:77], v226 offset:160
	ds_read_b128 v[78:81], v226 offset:192
	ds_read_b128 v[82:85], v226 offset:224
	ds_read_b128 v[66:69], v208 offset:57472
	v_add_f32_e32 v179, v173, v179
	v_add_f32_e32 v179, v176, v179
	v_add_f32_e32 v179, v172, v179
	v_add_f32_e32 v179, v174, v179
	v_add_f32_e32 v179, v170, v179
	v_add_f32_e32 v179, v171, v179
	s_waitcnt lgkmcnt(1)
	v_mfma_f32_32x32x16_bf16 v[70:85], v[102:105], v[158:161], v[70:85]
	ds_read_b128 v[102:105], v209 offset:49152
	ds_read_b128 v[110:113], v209 offset:57344
	ds_read_b128 v[180:183], v209 offset:49280
	v_add_f32_e32 v179, v165, v179
	v_add_f32_e32 v179, v168, v179
	v_exp_f32_e32 v128, v128
	v_exp_f32_e32 v129, v129
	v_exp_f32_e32 v126, v126
	s_waitcnt lgkmcnt(2)
	v_mfma_f32_32x32x16_bf16 v[86:101], v[102:105], v[154:157], v[86:101]
	ds_read_b128 v[102:105], v209 offset:57472
	ds_read_b128 v[184:187], v211 offset:49152
	ds_read_b128 v[188:191], v211 offset:49280
	ds_read_b128 v[204:207], v211 offset:57344
	ds_read_b128 v[230:233], v211 offset:57472
	ds_read_b128 v[234:237], v212 offset:49152
	ds_read_b128 v[238:241], v212 offset:49280
	v_exp_f32_e32 v127, v127
	v_exp_f32_e32 v124, v124
	v_exp_f32_e32 v125, v125
	v_exp_f32_e32 v122, v122
	v_exp_f32_e32 v123, v123
	v_exp_f32_e32 v120, v120
	s_waitcnt lgkmcnt(8)
	v_mfma_f32_32x32x16_bf16 v[70:85], v[110:113], v[154:157], v[70:85]
	ds_read_b128 v[110:113], v212 offset:57344
	ds_read_b128 v[242:245], v212 offset:57472
	v_exp_f32_e32 v121, v121
	v_exp_f32_e32 v118, v118
	v_exp_f32_e32 v119, v119
	v_exp_f32_e32 v116, v116
	v_exp_f32_e32 v117, v117
	v_exp_f32_e32 v114, v114
	s_waitcnt lgkmcnt(7)
	v_mfma_f32_32x32x16_bf16 v[86:101], v[184:187], v[150:153], v[86:101]
	v_exp_f32_e32 v115, v115
	s_sub_i32 s4, s36, 63
	s_waitcnt lgkmcnt(5)
	v_mfma_f32_32x32x16_bf16 v[70:85], v[204:207], v[150:153], v[70:85]
	s_waitcnt lgkmcnt(3)
	v_mfma_f32_32x32x16_bf16 v[86:101], v[234:237], v[146:149], v[86:101]
	s_waitcnt lgkmcnt(1)
; __device__ __forceinline__ void finishSM(f32x16& p0, f32x16& p1, float alpha, float& l_reg, bf16x8& pa0, bf16x8& pa1, bf16x8& pa2, bf16x8& pa3) {
;     for (int r = 0; r < 16; ++r) p1[r] = __builtin_amdgcn_exp2f(p1[r]);
;     float ps = 0; for (int r = 0; r < 16; ++r) ps += p0[r]; for (int r = 0; r < 16; ++r) ps += p1[r];
;     { auto rr = __builtin_amdgcn_permlane32_swap(__float_as_uint(ps), __float_as_uint(ps), false, false);
;       ps = __uint_as_float(rr[0]) + __uint_as_float(rr[1]); }
;     l_reg = l_reg * alpha + ps;
;     ...
;     PK4(p0, 0, pa0); PK4(p0, 8, pa1); PK4(p1, 0, pa2); PK4(p1, 8, pa3);
;     ...
; }
; template <int VB, bool SK>
; __device__ __forceinline__ void pv_tile(f32x16* o, int vb0, bf16x8 pa0, bf16x8 pa1, bf16x8 pa2, bf16x8 pa3, bool act) {
;     if (SK && !act) return;
;     ...
;     PV_D0(0); PV_D0(1); PV_D0(2); PV_D0(3);
	v_mfma_f32_32x32x16_bf16 v[70:85], v[110:113], v[146:149], v[70:85]
	v_add_f32_e32 v110, v163, v179
	v_add_f32_e32 v110, v166, v110
	v_add_f32_e32 v110, v162, v110
	v_add_f32_e32 v110, v169, v110
	v_add_f32_e32 v110, v164, v110
	v_add_f32_e32 v110, v167, v110
	v_add_f32_e32 v110, v128, v110
	v_mfma_f32_32x32x16_bf16 v[86:101], v[106:109], v[142:145], v[86:101]
	v_add_f32_e32 v106, v129, v110
	v_add_f32_e32 v106, v126, v106
	v_add_f32_e32 v106, v127, v106
	v_add_f32_e32 v106, v124, v106
	v_add_f32_e32 v106, v125, v106
	v_add_f32_e32 v106, v122, v106
	v_add_f32_e32 v106, v123, v106
	v_mfma_f32_32x32x16_bf16 v[70:85], v[66:69], v[142:145], v[70:85]
	v_add_f32_e32 v66, v120, v106
	v_add_f32_e32 v66, v121, v66
	v_add_f32_e32 v66, v118, v66
	v_add_f32_e32 v66, v119, v66
	v_add_f32_e32 v66, v116, v66
	v_add_f32_e32 v66, v117, v66
	v_add_f32_e32 v66, v114, v66
	v_mfma_f32_32x32x16_bf16 v[86:101], v[180:183], v[138:141], v[86:101]
	v_add_f32_e32 v228, v115, v66
	v_mov_b32_e32 v229, v228
	s_nop 1
	v_permlane32_swap_b32_e32 v228, v229
	v_cvt_pk_bf16_f32 v66, v175, v177
	v_cvt_pk_bf16_f32 v67, v173, v176
	v_cvt_pk_bf16_f32 v68, v172, v174
	v_mfma_f32_32x32x16_bf16 v[70:85], v[102:105], v[138:141], v[70:85]
	v_cvt_pk_bf16_f32 v69, v170, v171
	v_cvt_pk_bf16_f32 v102, v165, v168
	v_cvt_pk_bf16_f32 v103, v163, v166
	v_cvt_pk_bf16_f32 v104, v162, v169
	v_cvt_pk_bf16_f32 v105, v164, v167
	v_cvt_pk_bf16_f32 v106, v128, v129
	v_cvt_pk_bf16_f32 v107, v126, v127
	v_mfma_f32_32x32x16_bf16 v[86:101], v[188:191], v[134:137], v[86:101]
	v_cvt_pk_bf16_f32 v108, v124, v125
	v_cvt_pk_bf16_f32 v109, v122, v123
	v_cvt_pk_bf16_f32 v110, v120, v121
	v_cvt_pk_bf16_f32 v111, v118, v119
	v_cvt_pk_bf16_f32 v112, v116, v117
	v_cvt_pk_bf16_f32 v113, v114, v115
	v_permlane32_swap_b32_e32 v66, v68
	v_mfma_f32_32x32x16_bf16 v[70:85], v[230:233], v[134:137], v[70:85]
	v_permlane32_swap_b32_e32 v67, v69
	v_permlane32_swap_b32_e32 v102, v104
	v_permlane32_swap_b32_e32 v103, v105
	v_permlane32_swap_b32_e32 v106, v108
	v_mfma_f32_32x32x16_bf16 v[86:101], v[238:241], v[130:133], v[86:101]
	v_permlane32_swap_b32_e32 v107, v109
	v_permlane32_swap_b32_e32 v110, v112
	v_permlane32_swap_b32_e32 v111, v113
	s_waitcnt lgkmcnt(0)
	v_mfma_f32_32x32x16_bf16 v[70:85], v[242:245], v[130:133], v[70:85]
	ds_read_b64_tr_b16 v[114:115], v199 offset:0
	ds_read_b64_tr_b16 v[116:117], v199 offset:0x800
	ds_read_b64_tr_b16 v[118:119], v199 offset:0x1000
	ds_read_b64_tr_b16 v[120:121], v199 offset:0x1800
	ds_read_b64_tr_b16 v[122:123], v199 offset:0x2000
	ds_read_b64_tr_b16 v[124:125], v199 offset:0x2800
	ds_read_b64_tr_b16 v[126:127], v199 offset:0x3000
	ds_read_b64_tr_b16 v[128:129], v199 offset:0x3800
	s_waitcnt lgkmcnt(0)
	s_nop 0
	v_mfma_f32_32x32x16_bf16 v[50:65], v[66:69], v[114:117], v[50:65]
	ds_read_b64_tr_b16 v[114:115], v199 offset:0x200
	ds_read_b64_tr_b16 v[116:117], v199 offset:0xa00
	v_mfma_f32_32x32x16_bf16 v[50:65], v[102:105], v[118:121], v[50:65]
	ds_read_b64_tr_b16 v[118:119], v199 offset:0x1200
	ds_read_b64_tr_b16 v[120:121], v199 offset:0x1a00
	v_mfma_f32_32x32x16_bf16 v[50:65], v[106:109], v[122:125], v[50:65]
	ds_read_b64_tr_b16 v[122:123], v199 offset:0x2200
	ds_read_b64_tr_b16 v[124:125], v199 offset:0x2a00
	ds_read_b64_tr_b16 v[180:181], v199 offset:0x3200
	ds_read_b64_tr_b16 v[182:183], v199 offset:0x3a00
	s_waitcnt lgkmcnt(0)
	v_mfma_f32_32x32x16_bf16 v[50:65], v[110:113], v[126:129], v[50:65]
	v_mfma_f32_32x32x16_bf16 v[34:49], v[66:69], v[114:117], v[34:49]
	ds_read_b64_tr_b16 v[114:115], v199 offset:0x400
	ds_read_b64_tr_b16 v[116:117], v199 offset:0xc00
	v_mfma_f32_32x32x16_bf16 v[34:49], v[102:105], v[118:121], v[34:49]
	ds_read_b64_tr_b16 v[118:119], v199 offset:0x1400
	ds_read_b64_tr_b16 v[120:121], v199 offset:0x1c00
	v_mfma_f32_32x32x16_bf16 v[34:49], v[106:109], v[122:125], v[34:49]
	ds_read_b64_tr_b16 v[122:123], v199 offset:0x2400
	ds_read_b64_tr_b16 v[124:125], v199 offset:0x2c00
	ds_read_b64_tr_b16 v[126:127], v199 offset:0x3400
	ds_read_b64_tr_b16 v[128:129], v199 offset:0x3c00
	s_waitcnt lgkmcnt(0)
	v_mfma_f32_32x32x16_bf16 v[34:49], v[110:113], v[180:183], v[34:49]
	v_mfma_f32_32x32x16_bf16 v[18:33], v[66:69], v[114:117], v[18:33]
	ds_read_b64_tr_b16 v[114:115], v199 offset:0x600
	ds_read_b64_tr_b16 v[116:117], v199 offset:0xe00
	v_mfma_f32_32x32x16_bf16 v[18:33], v[102:105], v[118:121], v[18:33]
	ds_read_b64_tr_b16 v[118:119], v199 offset:0x1600
	ds_read_b64_tr_b16 v[120:121], v199 offset:0x1e00
	v_mfma_f32_32x32x16_bf16 v[18:33], v[106:109], v[122:125], v[18:33]
	ds_read_b64_tr_b16 v[122:123], v199 offset:0x2600
	ds_read_b64_tr_b16 v[124:125], v199 offset:0x2e00
	ds_read_b64_tr_b16 v[180:181], v199 offset:0x3600
	ds_read_b64_tr_b16 v[182:183], v199 offset:0x3e00
	s_waitcnt lgkmcnt(0)
	v_mfma_f32_32x32x16_bf16 v[18:33], v[110:113], v[126:129], v[18:33]
	v_mfma_f32_32x32x16_bf16 v[2:17], v[66:69], v[114:117], v[2:17]
	s_cmp_le_u32 s36, s15
	s_cselect_b64 s[20:21], -1, 0
	s_cmp_gt_i32 s4, s33
	s_cselect_b64 s[4:5], -1, 0
	s_and_b64 s[4:5], s[4:5], s[20:21]
	s_and_b64 vcc, exec, s[4:5]
	v_mfma_f32_32x32x16_bf16 v[2:17], v[102:105], v[118:121], v[2:17]
	v_mfma_f32_32x32x16_bf16 v[2:17], v[106:109], v[122:125], v[2:17]
	v_mfma_f32_32x32x16_bf16 v[2:17], v[110:113], v[180:183], v[2:17]
	s_cbranch_vccnz .LBB0_477
; __device__ __forceinline__ void mask_tile(f32x16& p0, f32x16& p1, int dq, unsigned W) {
;     const float NEG = -__builtin_inff();
; #pragma unroll
;     for (int r = 0; r < 16; ++r) {
;         const int c = (r & 3) + 8 * (r >> 2);
;         if ((unsigned)(dq - c) >= W) p0[r] = NEG;
;         if ((unsigned)(dq - c - 32) >= W) p1[r] = NEG;
;     }
; }
; __device__ __forceinline__ void partialSM(f32x16& p0, f32x16& p1, float& m_reg, float& mn, float& alpha) {
;     float pmax = p0[0]; for (int r = 1; r < 16; ++r) pmax = fmaxf(pmax, p0[r]); for (int r = 0; r < 16; ++r) pmax = fmaxf(pmax, p1[r]);
;     { auto rr = __builtin_amdgcn_permlane32_swap(__float_as_uint(pmax), __float_as_uint(pmax), false, false);
;       pmax = fmaxf(__uint_as_float(rr[0]), __uint_as_float(rr[1])); }
;     constexpr float C2 = 1.4426950408889634f * SCALE;
;     if (__builtin_expect(__all((pmax - m_reg) * SCALE <= THR), 1)) { mn = m_reg; alpha = 1.f; }
;     else { mn = fmaxf(m_reg, pmax); alpha = __builtin_amdgcn_exp2f((m_reg - mn) * C2); m_reg = mn; }
	v_add_u32_e32 v66, 0x7b, v225
	v_cmp_gt_u32_e32 vcc, s24, v66
	v_add_u32_e32 v66, 0x5b, v225
	s_nop 0
	v_cndmask_b32_e32 v86, v227, v86, vcc
	v_cmp_gt_u32_e32 vcc, s24, v66
	v_add_u32_e32 v66, 0x7a, v225
	s_nop 0
	v_cndmask_b32_e32 v70, v227, v70, vcc
	v_cmp_gt_u32_e32 vcc, s24, v66
	v_add_u32_e32 v66, 0x5a, v225
	s_nop 0
	v_cndmask_b32_e32 v87, v227, v87, vcc
	v_cmp_gt_u32_e32 vcc, s24, v66
	v_add_u32_e32 v66, 0x79, v225
	s_nop 0
	v_cndmask_b32_e32 v71, v227, v71, vcc
	v_cmp_gt_u32_e32 vcc, s24, v66
	v_add_u32_e32 v66, 0x59, v225
	s_nop 0
	v_cndmask_b32_e32 v88, v227, v88, vcc
	v_cmp_gt_u32_e32 vcc, s24, v66
	v_add_u32_e32 v66, 0x78, v225
	s_nop 0
	v_cndmask_b32_e32 v72, v227, v72, vcc
	v_cmp_gt_u32_e32 vcc, s24, v66
	v_add_u32_e32 v66, 0x58, v225
	s_nop 0
	v_cndmask_b32_e32 v89, v227, v89, vcc
	v_cmp_gt_u32_e32 vcc, s24, v66
	v_add_u32_e32 v66, 0x73, v225
	s_nop 0
	v_cndmask_b32_e32 v73, v227, v73, vcc
	v_cmp_gt_u32_e32 vcc, s24, v66
	v_add_u32_e32 v66, 0x53, v225
	s_nop 0
	v_cndmask_b32_e32 v90, v227, v90, vcc
	v_cmp_gt_u32_e32 vcc, s24, v66
	v_add_u32_e32 v66, 0x72, v225
	s_nop 0
	v_cndmask_b32_e32 v74, v227, v74, vcc
	v_cmp_gt_u32_e32 vcc, s24, v66
	v_add_u32_e32 v66, 0x52, v225
	s_nop 0
	v_cndmask_b32_e32 v91, v227, v91, vcc
	v_cmp_gt_u32_e32 vcc, s24, v66
	v_add_u32_e32 v66, 0x71, v225
	s_nop 0
	v_cndmask_b32_e32 v75, v227, v75, vcc
	v_cmp_gt_u32_e32 vcc, s24, v66
	v_add_u32_e32 v66, 0x51, v225
	s_nop 0
	v_cndmask_b32_e32 v92, v227, v92, vcc
	v_cmp_gt_u32_e32 vcc, s24, v66
	v_add_u32_e32 v66, 0x70, v225
	s_nop 0
	v_cndmask_b32_e32 v76, v227, v76, vcc
	v_cmp_gt_u32_e32 vcc, s24, v66
	v_add_u32_e32 v66, 0x50, v225
	s_nop 0
	v_cndmask_b32_e32 v93, v227, v93, vcc
	v_cmp_gt_u32_e32 vcc, s24, v66
	v_add_u32_e32 v66, 0x6b, v225
	s_nop 0
	v_cndmask_b32_e32 v77, v227, v77, vcc
	v_cmp_gt_u32_e32 vcc, s24, v66
	v_add_u32_e32 v66, 0x4b, v225
	s_nop 0
	v_cndmask_b32_e32 v94, v227, v94, vcc
	v_cmp_gt_u32_e32 vcc, s24, v66
	v_add_u32_e32 v66, 0x6a, v225
	s_nop 0
	v_cndmask_b32_e32 v78, v227, v78, vcc
	v_cmp_gt_u32_e32 vcc, s24, v66
	v_add_u32_e32 v66, 0x4a, v225
	s_nop 0
	v_cndmask_b32_e32 v95, v227, v95, vcc
	v_cmp_gt_u32_e32 vcc, s24, v66
	v_add_u32_e32 v66, 0x69, v225
	s_nop 0
	v_cndmask_b32_e32 v79, v227, v79, vcc
	v_cmp_gt_u32_e32 vcc, s24, v66
	v_add_u32_e32 v66, 0x49, v225
	s_nop 0
	v_cndmask_b32_e32 v96, v227, v96, vcc
	v_cmp_gt_u32_e32 vcc, s24, v66
	v_add_u32_e32 v66, 0x68, v225
	s_nop 0
	v_cndmask_b32_e32 v80, v227, v80, vcc
	v_cmp_gt_u32_e32 vcc, s24, v66
	v_add_u32_e32 v66, 0x48, v225
	s_nop 0
	v_cndmask_b32_e32 v97, v227, v97, vcc
	v_cmp_gt_u32_e32 vcc, s24, v66
	v_add_u32_e32 v66, 0x63, v225
	s_nop 0
	v_cndmask_b32_e32 v81, v227, v81, vcc
	v_cmp_gt_u32_e32 vcc, s24, v66
	v_add_u32_e32 v66, 0x43, v225
	s_nop 0
	v_cndmask_b32_e32 v98, v227, v98, vcc
	v_cmp_gt_u32_e32 vcc, s24, v66
	v_add_u32_e32 v66, 0x62, v225
	s_nop 0
	v_cndmask_b32_e32 v82, v227, v82, vcc
	v_cmp_gt_u32_e32 vcc, s24, v66
	v_add_u32_e32 v66, 0x42, v225
	s_nop 0
	v_cndmask_b32_e32 v99, v227, v99, vcc
	v_cmp_gt_u32_e32 vcc, s24, v66
	v_add_u32_e32 v66, 0x61, v225
	s_nop 0
	v_cndmask_b32_e32 v83, v227, v83, vcc
	v_cmp_gt_u32_e32 vcc, s24, v66
	v_add_u32_e32 v66, 0x41, v225
	s_nop 0
	v_cndmask_b32_e32 v100, v227, v100, vcc
	v_cmp_gt_u32_e32 vcc, s24, v66
	v_add_u32_e32 v66, 0x60, v225
	s_nop 0
	v_cndmask_b32_e32 v84, v227, v84, vcc
	v_cmp_gt_u32_e32 vcc, s24, v66
	v_add_u32_e32 v66, 64, v225
	s_nop 0
	v_cndmask_b32_e32 v101, v227, v101, vcc
	v_cmp_gt_u32_e32 vcc, s24, v66
	s_nop 1
	v_cndmask_b32_e32 v85, v227, v85, vcc
.LBB0_477:
	v_max_f32_e32 v66, v87, v87
	v_max_f32_e32 v67, v86, v86
	v_max_f32_e32 v66, v67, v66
	v_max3_f32 v66, v66, v88, v89
	v_max3_f32 v66, v66, v90, v91
	v_max3_f32 v66, v66, v92, v93
	v_max3_f32 v66, v66, v94, v95
	v_max3_f32 v66, v66, v96, v97
	v_max3_f32 v66, v66, v98, v99
	v_max3_f32 v66, v66, v100, v101
	v_max3_f32 v66, v66, v70, v71
	v_max3_f32 v66, v66, v72, v73
	v_max3_f32 v66, v66, v74, v75
	v_max3_f32 v66, v66, v76, v77
	v_max3_f32 v66, v66, v78, v79
	v_max3_f32 v66, v66, v80, v81
	v_max3_f32 v66, v66, v82, v83
	v_max3_f32 v66, v66, v84, v85
	v_mov_b32_e32 v67, v66
	s_nop 1
	v_permlane32_swap_b32_e32 v66, v67
	v_max_f32_e32 v67, v67, v67
	v_max_f32_e32 v66, v66, v66
	v_max_f32_e32 v66, v66, v67
	v_max_f32_e32 v68, v178, v178
	v_sub_f32_e32 v67, v66, v178
	v_max_f32_e32 v66, v68, v66
	v_sub_f32_e32 v68, v178, v66
	v_mul_f32_e32 v68, 0x3e0293ee, v68
	v_mul_f32_e32 v67, 0x3db504f3, v67
	v_exp_f32_e32 v68, v68
	v_cmp_ge_f32_e32 vcc, s38, v67
	s_cmp_eq_u64 vcc, exec
	s_cselect_b64 s[4:5], -1, 0
	s_barrier
	v_cndmask_b32_e64 v230, v68, 1.0, s[4:5]
	v_cmp_gt_f32_e32 vcc, 1.0, v230
	s_add_u32 s98, s0, 0x9640000
	s_addc_u32 s99, s1, 0
	s_lshl_b32 s100, s75, 10
	s_add_i32 m0, s100, 0x0
	s_nop 0
	global_load_lds_dwordx4 v254, s[98:99]
	s_add_u32 s98, s98, 0x10000
	s_addc_u32 s99, s99, 0
	s_add_i32 m0, m0, 0x2000
	s_nop 0
	global_load_lds_dwordx4 v254, s[98:99]
	s_waitcnt vmcnt(2)
	s_cbranch_vccz .LBB0_481
	s_and_saveexec_b64 s[20:21], s[2:3]
	ds_write_b32 v220, v230 offset:128
	s_or_b64 exec, exec, s[20:21]
	s_waitcnt lgkmcnt(0)
	ds_read_b128 v[102:105], v219 offset:224
	ds_read_b128 v[106:109], v219 offset:192
	ds_read_b128 v[110:113], v219 offset:160
	ds_read_b128 v[114:117], v219 offset:128
	s_waitcnt lgkmcnt(3)
	v_pk_mul_f32 v[64:65], v[64:65], v[104:105]
	s_waitcnt lgkmcnt(2)
	v_pk_mul_f32 v[60:61], v[60:61], v[108:109]
	s_waitcnt lgkmcnt(1)
	v_pk_mul_f32 v[56:57], v[56:57], v[112:113]
	s_waitcnt lgkmcnt(0)
	v_pk_mul_f32 v[52:53], v[52:53], v[116:117]
	v_pk_mul_f32 v[62:63], v[62:63], v[102:103]
	v_pk_mul_f32 v[58:59], v[58:59], v[106:107]
	v_pk_mul_f32 v[54:55], v[54:55], v[110:111]
	v_pk_mul_f32 v[50:51], v[50:51], v[114:115]
	v_pk_mul_f32 v[48:49], v[48:49], v[104:105]
	v_pk_mul_f32 v[44:45], v[44:45], v[108:109]
	v_pk_mul_f32 v[40:41], v[40:41], v[112:113]
	v_pk_mul_f32 v[36:37], v[36:37], v[116:117]
	v_pk_mul_f32 v[46:47], v[46:47], v[102:103]
	v_pk_mul_f32 v[42:43], v[42:43], v[106:107]
	v_pk_mul_f32 v[38:39], v[38:39], v[110:111]
	v_pk_mul_f32 v[34:35], v[34:35], v[114:115]
	v_pk_mul_f32 v[32:33], v[32:33], v[104:105]
	v_pk_mul_f32 v[28:29], v[28:29], v[108:109]
	v_pk_mul_f32 v[24:25], v[24:25], v[112:113]
	v_pk_mul_f32 v[20:21], v[20:21], v[116:117]
	v_pk_mul_f32 v[30:31], v[30:31], v[102:103]
	v_pk_mul_f32 v[26:27], v[26:27], v[106:107]
	v_pk_mul_f32 v[22:23], v[22:23], v[110:111]
	v_pk_mul_f32 v[18:19], v[18:19], v[114:115]
	v_pk_mul_f32 v[16:17], v[16:17], v[104:105]
	v_pk_mul_f32 v[12:13], v[12:13], v[108:109]
	v_pk_mul_f32 v[8:9], v[8:9], v[112:113]
	v_pk_mul_f32 v[4:5], v[4:5], v[116:117]
	v_pk_mul_f32 v[14:15], v[14:15], v[102:103]
	v_pk_mul_f32 v[10:11], v[10:11], v[106:107]
	v_pk_mul_f32 v[6:7], v[6:7], v[110:111]
	v_pk_mul_f32 v[2:3], v[2:3], v[114:115]
; __device__ __forceinline__ void partialSM(f32x16& p0, f32x16& p1, float& m_reg, float& mn, float& alpha) {
;     float pmax = p0[0]; for (int r = 1; r < 16; ++r) pmax = fmaxf(pmax, p0[r]); for (int r = 0; r < 16; ++r) pmax = fmaxf(pmax, p1[r]);
;     { auto rr = __builtin_amdgcn_permlane32_swap(__float_as_uint(pmax), __float_as_uint(pmax), false, false);
;       pmax = fmaxf(__uint_as_float(rr[0]), __uint_as_float(rr[1])); }
;     constexpr float C2 = 1.4426950408889634f * SCALE;
;     if (__builtin_expect(__all((pmax - m_reg) * SCALE <= THR), 1)) { mn = m_reg; alpha = 1.f; }
;     else { mn = fmaxf(m_reg, pmax); alpha = __builtin_amdgcn_exp2f((m_reg - mn) * C2); m_reg = mn; }
;     const float mnL = -mn * C2;
;     for (int r = 0; r < 16; ++r) p0[r] = fmaf(p0[r], C2, mnL); for (int r = 0; r < 16; ++r) p1[r] = fmaf(p1[r], C2, mnL);
;     for (int r = 0; r < 16; ++r) p0[r] = __builtin_amdgcn_exp2f(p0[r]);
.LBB0_481:
	v_cndmask_b32_e64 v231, v66, v178, s[4:5]
	v_mul_f32_e32 v178, 0xbe0293ee, v231
	v_fmamk_f32 v66, v86, 0x3e0293ee, v178
	v_fmamk_f32 v67, v87, 0x3e0293ee, v178
	v_fmamk_f32 v68, v88, 0x3e0293ee, v178
	v_fmamk_f32 v69, v89, 0x3e0293ee, v178
	v_fmamk_f32 v102, v90, 0x3e0293ee, v178
	v_fmamk_f32 v103, v91, 0x3e0293ee, v178
	v_fmamk_f32 v104, v92, 0x3e0293ee, v178
	v_fmamk_f32 v105, v93, 0x3e0293ee, v178
	v_fmamk_f32 v106, v94, 0x3e0293ee, v178
	v_fmamk_f32 v107, v95, 0x3e0293ee, v178
	v_fmamk_f32 v108, v96, 0x3e0293ee, v178
	v_fmamk_f32 v109, v97, 0x3e0293ee, v178
	v_fmamk_f32 v98, v98, 0x3e0293ee, v178
	v_fmamk_f32 v99, v99, 0x3e0293ee, v178
	v_fmamk_f32 v100, v100, 0x3e0293ee, v178
	v_fmamk_f32 v101, v101, 0x3e0293ee, v178
	v_fmamk_f32 v86, v70, 0x3e0293ee, v178
	v_fmamk_f32 v95, v71, 0x3e0293ee, v178
	v_fmamk_f32 v96, v72, 0x3e0293ee, v178
	v_fmamk_f32 v97, v73, 0x3e0293ee, v178
	v_fmamk_f32 v179, v74, 0x3e0293ee, v178
	v_fmamk_f32 v87, v75, 0x3e0293ee, v178
	v_fmamk_f32 v88, v76, 0x3e0293ee, v178
	v_fmamk_f32 v89, v77, 0x3e0293ee, v178
	v_fmamk_f32 v90, v78, 0x3e0293ee, v178
	v_fmamk_f32 v91, v79, 0x3e0293ee, v178
	v_fmamk_f32 v92, v80, 0x3e0293ee, v178
	v_fmamk_f32 v93, v81, 0x3e0293ee, v178
	v_exp_f32_e32 v66, v66
	v_exp_f32_e32 v67, v67
	v_exp_f32_e32 v68, v68
	v_exp_f32_e32 v69, v69
	v_exp_f32_e32 v70, v102
	v_exp_f32_e32 v71, v103
	v_exp_f32_e32 v72, v104
	v_exp_f32_e32 v73, v105
	v_exp_f32_e32 v74, v106
	v_exp_f32_e32 v75, v107
	v_exp_f32_e32 v76, v108
	v_exp_f32_e32 v77, v109
	v_exp_f32_e32 v78, v98
	v_exp_f32_e32 v79, v99
	v_exp_f32_e32 v80, v100
	v_exp_f32_e32 v81, v101
	v_fmamk_f32 v94, v82, 0x3e0293ee, v178
	v_fmamk_f32 v180, v83, 0x3e0293ee, v178
	v_fmamk_f32 v181, v84, 0x3e0293ee, v178
	v_fmac_f32_e32 v178, 0x3e0293ee, v85
	s_waitcnt lgkmcnt(0)
	s_barrier
	s_add_i32 s100, s35, 1
	s_cmp_lt_i32 s100, s34
	s_cbranch_scc0 .Lattn_k2skip_1
	s_add_u32 s98, s0, 0x7660000
	s_addc_u32 s99, s1, 0
	s_lshl_b32 s100, s75, 10
	s_add_i32 m0, s100, 0xc000
	s_nop 0
	global_load_lds_dwordx4 v253, s[98:99]
	s_add_u32 s98, s98, 0x10000
	s_addc_u32 s99, s99, 0
	s_add_i32 m0, m0, 0x2000
	s_nop 0
	global_load_lds_dwordx4 v253, s[98:99]
; __device__ __forceinline__ void finishSM(f32x16& p0, f32x16& p1, float alpha, float& l_reg, bf16x8& pa0, bf16x8& pa1, bf16x8& pa2, bf16x8& pa3) {
;     for (int r = 0; r < 16; ++r) p1[r] = __builtin_amdgcn_exp2f(p1[r]);
;     float ps = 0; for (int r = 0; r < 16; ++r) ps += p0[r]; for (int r = 0; r < 16; ++r) ps += p1[r];
;     { auto rr = __builtin_amdgcn_permlane32_swap(__float_as_uint(ps), __float_as_uint(ps), false, false);
;       ps = __uint_as_float(rr[0]) + __uint_as_float(rr[1]); }
;     l_reg = l_reg * alpha + ps;
;     ...
;     PK4(p0, 0, pa0); PK4(p0, 8, pa1); PK4(p1, 0, pa2); PK4(p1, 8, pa3);
;     ...
; }
; template <int KB, bool SK, bool BIAS>
; __device__ __forceinline__ void qkt(f32x16& p0, f32x16& p1, const char* K_lds, int r32, int hi, const bf16x8* qr, bool act, const float* bl) {
;     if (SK && !act) { const float NEG = -__builtin_inff();
; #pragma unroll
;         for (int r = 0; r < 16; ++r) { p0[r] = NEG; p1[r] = NEG; } return; }
;     if constexpr (BIAS) {
; #pragma unroll
;         for (int g_ = 0; g_ < 4; ++g_) { const f32x4 t0 = *(const f32x4*)(bl + 8 * g_), t1 = *(const f32x4*)(bl + 32 + 8 * g_);
;             p0[4 * g_] = t0[0]; p0[4 * g_ + 1] = t0[1]; p0[4 * g_ + 2] = t0[2]; p0[4 * g_ + 3] = t0[3]; p1[4 * g_] = t1[0]; p1[4 * g_ + 1] = t1[1]; p1[4 * g_ + 2] = t1[2]; p1[4 * g_ + 3] = t1[3]; }
;     } else { p0 = f32x16{}; p1 = f32x16{}; }
;     const char* kb[4];
; #pragma unroll
;     for (int dd = 0; dd < 4; ++dd) kb[dd] = K_lds + KB * SHM_K + KSWZ(r32, (dd * 16 + hi * 8) * 2);
; #pragma unroll
;     for (int d0 = 0; d0 < 8; ++d0) { const char* a = kb[d0 & 3] + (d0 >> 2) * 128;
;         bf16x8 b0 = *reinterpret_cast<const bf16x8*>(a);
;         bf16x8 b1 = *reinterpret_cast<const bf16x8*>(a + 32 * 256);
;         p0 = __builtin_amdgcn_mfma_f32_32x32x16_bf16(b0, qr[d0], p0, 0, 0, 0);
;         p1 = __builtin_amdgcn_mfma_f32_32x32x16_bf16(b1, qr[d0], p1, 0, 0, 0); }
.Lattn_k2skip_1:
	ds_read_b128 v[114:117], v226 offset:256
	ds_read_b128 v[118:121], v226 offset:288
	ds_read_b128 v[98:101], v226 offset:384
	ds_read_b128 v[102:105], v226 offset:416
	ds_read_b128 v[122:125], v226 offset:320
	ds_read_b128 v[106:109], v226 offset:448
	ds_read_b128 v[126:129], v226 offset:352
	ds_read_b128 v[110:113], v226 offset:480
	ds_read_b128 v[82:85], v208 offset:32768
	ds_read_b128 v[182:185], v208 offset:40960
	v_exp_f32_e32 v87, v87
	v_exp_f32_e32 v88, v88
	v_exp_f32_e32 v89, v89
	s_waitcnt lgkmcnt(1)
	v_mfma_f32_32x32x16_bf16 v[114:129], v[82:85], v[158:161], v[114:129]
	v_exp_f32_e32 v90, v90
	v_exp_f32_e32 v91, v91
	v_exp_f32_e32 v92, v92
	v_exp_f32_e32 v93, v93
	v_exp_f32_e32 v94, v94
	s_waitcnt lgkmcnt(0)
	v_mfma_f32_32x32x16_bf16 v[98:113], v[182:185], v[158:161], v[98:113]
	ds_read_b128 v[82:85], v209 offset:32768
	ds_read_b128 v[182:185], v209 offset:40960
	s_waitcnt lgkmcnt(1)
	v_mfma_f32_32x32x16_bf16 v[114:129], v[82:85], v[154:157], v[114:129]
	s_waitcnt lgkmcnt(0)
	v_mfma_f32_32x32x16_bf16 v[98:113], v[182:185], v[154:157], v[98:113]
	ds_read_b128 v[82:85], v211 offset:32768
	ds_read_b128 v[182:185], v211 offset:40960
	s_waitcnt lgkmcnt(1)
	v_mfma_f32_32x32x16_bf16 v[114:129], v[82:85], v[150:153], v[114:129]
	s_waitcnt lgkmcnt(0)
	v_mfma_f32_32x32x16_bf16 v[98:113], v[182:185], v[150:153], v[98:113]
	ds_read_b128 v[82:85], v212 offset:32768
	ds_read_b128 v[182:185], v212 offset:40960
	s_waitcnt lgkmcnt(1)
	v_mfma_f32_32x32x16_bf16 v[114:129], v[82:85], v[146:149], v[114:129]
	s_waitcnt lgkmcnt(0)
	v_mfma_f32_32x32x16_bf16 v[98:113], v[182:185], v[146:149], v[98:113]
	ds_read_b128 v[82:85], v208 offset:32896
	ds_read_b128 v[182:185], v208 offset:41088
	s_waitcnt lgkmcnt(1)
	v_mfma_f32_32x32x16_bf16 v[114:129], v[82:85], v[142:145], v[114:129]
	s_waitcnt lgkmcnt(0)
	v_mfma_f32_32x32x16_bf16 v[98:113], v[182:185], v[142:145], v[98:113]
	ds_read_b128 v[82:85], v209 offset:32896
	ds_read_b128 v[182:185], v209 offset:41088
	s_waitcnt lgkmcnt(1)
	v_mfma_f32_32x32x16_bf16 v[114:129], v[82:85], v[138:141], v[114:129]
	s_waitcnt lgkmcnt(0)
	v_mfma_f32_32x32x16_bf16 v[98:113], v[182:185], v[138:141], v[98:113]
	ds_read_b128 v[82:85], v211 offset:32896
	ds_read_b128 v[182:185], v211 offset:41088
	s_waitcnt lgkmcnt(1)
	v_mfma_f32_32x32x16_bf16 v[114:129], v[82:85], v[134:137], v[114:129]
	s_waitcnt lgkmcnt(0)
	v_mfma_f32_32x32x16_bf16 v[98:113], v[182:185], v[134:137], v[98:113]
	ds_read_b128 v[82:85], v212 offset:32896
	ds_read_b128 v[182:185], v212 offset:41088
	s_waitcnt lgkmcnt(1)
	v_mfma_f32_32x32x16_bf16 v[114:129], v[82:85], v[130:133], v[114:129]
	v_exp_f32_e32 v85, v97
	v_exp_f32_e32 v97, v178
	v_add_f32_e32 v178, 0, v66
	v_add_f32_e32 v178, v67, v178
	v_add_f32_e32 v178, v68, v178
	v_add_f32_e32 v178, v69, v178
	v_add_f32_e32 v178, v70, v178
	v_add_f32_e32 v178, v71, v178
	v_add_f32_e32 v178, v72, v178
	v_add_f32_e32 v178, v73, v178
	v_add_f32_e32 v178, v74, v178
	v_add_f32_e32 v178, v75, v178
	v_add_f32_e32 v178, v76, v178
	v_add_f32_e32 v178, v77, v178
	v_exp_f32_e32 v82, v86
	v_add_f32_e32 v178, v78, v178
	v_exp_f32_e32 v83, v95
	v_add_f32_e32 v178, v79, v178
	v_exp_f32_e32 v84, v96
	v_add_f32_e32 v178, v80, v178
	v_add_f32_e32 v178, v81, v178
	v_exp_f32_e32 v86, v179
	v_add_f32_e32 v178, v82, v178
	v_add_f32_e32 v178, v83, v178
	v_add_f32_e32 v178, v84, v178
	v_add_f32_e32 v178, v85, v178
	v_add_f32_e32 v178, v86, v178
	v_add_f32_e32 v178, v87, v178
	v_add_f32_e32 v178, v88, v178
	v_add_f32_e32 v178, v89, v178
	v_add_f32_e32 v178, v90, v178
	v_exp_f32_e32 v95, v180
	v_add_f32_e32 v178, v91, v178
	s_waitcnt lgkmcnt(0)
	v_mfma_f32_32x32x16_bf16 v[98:113], v[182:185], v[130:133], v[98:113]
	v_exp_f32_e32 v96, v181
	v_add_f32_e32 v178, v92, v178
	v_add_f32_e32 v178, v93, v178
	v_add_f32_e32 v178, v94, v178
	v_add_f32_e32 v178, v95, v178
	v_add_f32_e32 v178, v96, v178
	v_add_f32_e32 v232, v97, v178
	v_mov_b32_e32 v233, v232
	v_cvt_pk_bf16_f32 v178, v66, v67
	v_cvt_pk_bf16_f32 v179, v68, v69
	v_cvt_pk_bf16_f32 v180, v70, v71
	v_cvt_pk_bf16_f32 v181, v72, v73
	v_cvt_pk_bf16_f32 v182, v74, v75
	v_cvt_pk_bf16_f32 v183, v76, v77
	v_cvt_pk_bf16_f32 v184, v78, v79
	v_cvt_pk_bf16_f32 v185, v80, v81
	v_cvt_pk_bf16_f32 v186, v82, v83
	v_cvt_pk_bf16_f32 v187, v84, v85
	v_cvt_pk_bf16_f32 v188, v86, v87
	v_cvt_pk_bf16_f32 v189, v88, v89
	v_cvt_pk_bf16_f32 v190, v90, v91
	v_cvt_pk_bf16_f32 v191, v92, v93
	v_cvt_pk_bf16_f32 v192, v94, v95
	v_cvt_pk_bf16_f32 v193, v96, v97
	s_nop 1
	v_permlane32_swap_b32_e32 v232, v233
	v_permlane32_swap_b32_e32 v178, v180
	v_permlane32_swap_b32_e32 v179, v181
	v_permlane32_swap_b32_e32 v182, v184
	v_permlane32_swap_b32_e32 v183, v185
	v_permlane32_swap_b32_e32 v186, v188
	v_permlane32_swap_b32_e32 v187, v189
	v_permlane32_swap_b32_e32 v190, v192
	v_permlane32_swap_b32_e32 v191, v193
	s_add_i32 s4, s35, 1
	s_cmp_lt_i32 s4, s34
	s_cselect_b64 s[20:21], -1, 0
	s_cmp_ge_i32 s4, s34
	s_cbranch_scc1 .LBB0_483

; __device__ __forceinline__ void partialSM(f32x16& p0, f32x16& p1, float& m_reg, float& mn, float& alpha) {
;     float pmax = p0[0]; for (int r = 1; r < 16; ++r) pmax = fmaxf(pmax, p0[r]); for (int r = 0; r < 16; ++r) pmax = fmaxf(pmax, p1[r]);
;     { auto rr = __builtin_amdgcn_permlane32_swap(__float_as_uint(pmax), __float_as_uint(pmax), false, false);
;       pmax = fmaxf(__uint_as_float(rr[0]), __uint_as_float(rr[1])); }
;     constexpr float C2 = 1.4426950408889634f * SCALE;
;     if (__builtin_expect(__all((pmax - m_reg) * SCALE <= THR), 1)) { mn = m_reg; alpha = 1.f; }
;     else { mn = fmaxf(m_reg, pmax); alpha = __builtin_amdgcn_exp2f((m_reg - mn) * C2); m_reg = mn; }
.LBB0_485:
	v_max_f32_e32 v178, v115, v115
	v_max_f32_e32 v179, v114, v114
	v_max_f32_e32 v178, v179, v178
	v_max3_f32 v178, v178, v116, v117
	v_max3_f32 v178, v178, v118, v119
	v_max3_f32 v178, v178, v120, v121
	v_max3_f32 v178, v178, v122, v123
	v_max3_f32 v178, v178, v124, v125
	v_max3_f32 v178, v178, v126, v127
	v_max3_f32 v178, v178, v128, v129
	v_max3_f32 v178, v178, v98, v99
	v_max3_f32 v178, v178, v100, v101
	v_max3_f32 v178, v178, v102, v103
	v_max3_f32 v178, v178, v104, v105
	v_max3_f32 v178, v178, v106, v107
	v_max3_f32 v178, v178, v108, v109
	v_max3_f32 v178, v178, v110, v111
	v_max3_f32 v178, v178, v112, v113
	v_mov_b32_e32 v179, v178
	s_nop 1
	v_permlane32_swap_b32_e32 v178, v179
	v_max_f32_e32 v179, v179, v179
	v_max_f32_e32 v178, v178, v178
	v_max_f32_e32 v178, v178, v179
	v_sub_f32_e32 v179, v178, v231
	v_mul_f32_e32 v179, 0x3db504f3, v179
	v_cmp_ge_f32_e32 vcc, s38, v179
	s_cmp_eq_u64 vcc, exec
	s_cselect_b64 s[4:5], -1, 0
	s_andn2_b64 vcc, exec, s[20:21]
	s_barrier
	s_cbranch_vccnz .Lattn_vskip_1
	s_add_u32 s98, s0, 0x9660000
	s_addc_u32 s99, s1, 0
	s_lshl_b32 s100, s75, 10
	s_add_i32 m0, s100, 0x4000
	s_nop 0
	global_load_lds_dwordx4 v254, s[98:99]
	s_add_u32 s98, s98, 0x10000
	s_addc_u32 s99, s99, 0
	s_add_i32 m0, m0, 0x2000
	s_nop 0
	global_load_lds_dwordx4 v254, s[98:99]
	s_waitcnt vmcnt(2)
	s_branch .LBB0_487

.LBB0_487:
	v_max_f32_e32 v162, v231, v231
	v_max_f32_e32 v162, v162, v178
	v_sub_f32_e32 v163, v231, v162
	v_mul_f32_e32 v163, 0x3e0293ee, v163
	v_exp_f32_e32 v163, v163
	s_nop 0
	v_cndmask_b32_e64 v179, v163, 1.0, s[4:5]
	v_cmp_gt_f32_e32 vcc, 1.0, v179
	s_cbranch_vccz .LBB0_474
	s_and_saveexec_b64 s[20:21], s[2:3]
	s_cbranch_execz .LBB0_473
	ds_write_b32 v220, v179 offset:128
	s_branch .LBB0_473

; #define SBAR() __builtin_amdgcn_sched_barrier(0)
; #define BL(t) (bias0 + KBASE(t))
; #define ACT(t) (KBASE(t) <= qlo + QBLK - 1 && KBASE(t) + KVBLK - 1 >= qlo - W + 1)
; template <int KB, bool SK, bool BIAS>
; __device__ __forceinline__ void qkt(f32x16& p0, f32x16& p1, const char* K_lds, int r32, int hi, const bf16x8* qr, bool act, const float* bl) {
;     if (SK && !act) { const float NEG = -__builtin_inff();
; #pragma unroll
;         for (int r = 0; r < 16; ++r) { p0[r] = NEG; p1[r] = NEG; } return; }
;     if constexpr (BIAS) {
; #pragma unroll
;         for (int g_ = 0; g_ < 4; ++g_) { const f32x4 t0 = *(const f32x4*)(bl + 8 * g_), t1 = *(const f32x4*)(bl + 32 + 8 * g_);
;             p0[4 * g_] = t0[0]; p0[4 * g_ + 1] = t0[1]; p0[4 * g_ + 2] = t0[2]; p0[4 * g_ + 3] = t0[3]; p1[4 * g_] = t1[0]; p1[4 * g_ + 1] = t1[1]; p1[4 * g_ + 2] = t1[2]; p1[4 * g_ + 3] = t1[3]; }
;     } else { p0 = f32x16{}; p1 = f32x16{}; }
;     const char* kb[4];
; #pragma unroll
;     for (int dd = 0; dd < 4; ++dd) kb[dd] = K_lds + KB * SHM_K + KSWZ(r32, (dd * 16 + hi * 8) * 2);
; #pragma unroll
;     for (int d0 = 0; d0 < 8; ++d0) { const char* a = kb[d0 & 3] + (d0 >> 2) * 128;
;         bf16x8 b0 = *reinterpret_cast<const bf16x8*>(a);
;         bf16x8 b1 = *reinterpret_cast<const bf16x8*>(a + 32 * 256);
;         p0 = __builtin_amdgcn_mfma_f32_32x32x16_bf16(b0, qr[d0], p0, 0, 0, 0);
;         p1 = __builtin_amdgcn_mfma_f32_32x32x16_bf16(b1, qr[d0], p1, 0, 0, 0); }
; template <class TIn, class TOut, int QS, int KS, int OS, bool BIAS, bool PREF = true>
; __device__ __forceinline__ void causal_swa_block(const BlockRef<TIn, TOut>& cur, const BlockRef<TIn, TOut>& nxt, int skv, int W, char* lds, Seam<TIn>& S) {
;     ...
;     const bool even = (NT & 1) == 0;
;     if (even) { SBAR(); qkt<1, SK, BIAS>(pB0, pB1, K_lds, r32, hi, S.qr, ACT(NT - 1), BL(NT - 1)); SBAR(); }
.LBB0_493:
	s_waitcnt vmcnt(0)
	s_bitcmp0_b32 s34, 0
	s_cselect_b64 s[0:1], -1, 0
	s_mov_b32 s19, 0
	s_and_b64 vcc, exec, s[0:1]
	s_cbranch_vccz .LBB0_495
	v_lshl_add_u32 v94, s28, 8, v210
	v_add_u32_e32 v66, 0xffffff00, v94
	v_add_u32_e32 v70, 0xffffff80, v94
	ds_read_b128 v[66:69], v66
	ds_read_b128 v[82:85], v70
	v_add_u32_e32 v70, 0xffffff20, v94
	v_add_u32_e32 v74, 0xffffffa0, v94
	ds_read_b128 v[70:73], v70
	ds_read_b128 v[86:89], v74
	ds_read_b128 v[98:101], v208 offset:49152
	v_add_u32_e32 v74, 0xffffff40, v94
	v_subrev_u32_e32 v90, 64, v94
	v_add_u32_e32 v75, 0xffffff60, v94
	ds_read_b128 v[78:81], v75
	ds_read_b128 v[74:77], v74
	ds_read_b128 v[90:93], v90
	v_subrev_u32_e32 v94, 32, v94
	ds_read_b128 v[94:97], v94
	ds_read_b128 v[102:105], v208 offset:49280
	s_waitcnt lgkmcnt(3)
	v_mfma_f32_32x32x16_bf16 v[66:81], v[98:101], v[158:161], v[66:81]
	ds_read_b128 v[98:101], v208 offset:57344
	ds_read_b128 v[106:109], v208 offset:57472
	s_waitcnt lgkmcnt(1)
	v_mfma_f32_32x32x16_bf16 v[82:97], v[98:101], v[158:161], v[82:97]
	ds_read_b128 v[98:101], v209 offset:49152
	ds_read_b128 v[110:113], v209 offset:49280
	s_waitcnt lgkmcnt(1)
	v_mfma_f32_32x32x16_bf16 v[66:81], v[98:101], v[154:157], v[66:81]
	ds_read_b128 v[98:101], v209 offset:57344
	ds_read_b128 v[158:161], v209 offset:57472
	s_waitcnt lgkmcnt(1)
	v_mfma_f32_32x32x16_bf16 v[82:97], v[98:101], v[154:157], v[82:97]
	ds_read_b128 v[98:101], v211 offset:49152
	ds_read_b128 v[154:157], v211 offset:49280
	s_waitcnt lgkmcnt(1)
	v_mfma_f32_32x32x16_bf16 v[66:81], v[98:101], v[150:153], v[66:81]
	ds_read_b128 v[98:101], v211 offset:57344
	ds_read_b128 v[180:183], v211 offset:57472
	s_waitcnt lgkmcnt(1)
	v_mfma_f32_32x32x16_bf16 v[82:97], v[98:101], v[150:153], v[82:97]
	ds_read_b128 v[98:101], v212 offset:49152
	ds_read_b128 v[150:153], v212 offset:49280
	s_waitcnt lgkmcnt(1)
	v_mfma_f32_32x32x16_bf16 v[66:81], v[98:101], v[146:149], v[66:81]
	ds_read_b128 v[98:101], v212 offset:57344
	ds_read_b128 v[184:187], v212 offset:57472
	s_waitcnt lgkmcnt(1)
	v_mfma_f32_32x32x16_bf16 v[82:97], v[98:101], v[146:149], v[82:97]
	v_mfma_f32_32x32x16_bf16 v[66:81], v[102:105], v[142:145], v[66:81]
	v_mfma_f32_32x32x16_bf16 v[82:97], v[106:109], v[142:145], v[82:97]
	v_mfma_f32_32x32x16_bf16 v[66:81], v[110:113], v[138:141], v[66:81]
	v_mfma_f32_32x32x16_bf16 v[82:97], v[158:161], v[138:141], v[82:97]
	v_mfma_f32_32x32x16_bf16 v[66:81], v[154:157], v[134:137], v[66:81]
	v_mfma_f32_32x32x16_bf16 v[82:97], v[180:183], v[134:137], v[82:97]
	v_mfma_f32_32x32x16_bf16 v[66:81], v[150:153], v[130:133], v[66:81]
	s_waitcnt lgkmcnt(0)
	v_mfma_f32_32x32x16_bf16 v[82:97], v[184:187], v[130:133], v[82:97]

; __device__ __forceinline__ int v_st(int k, int c) { const int kk = (k & ~0xC) | ((k & 4) << 1) | ((k & 8) >> 1); return ((kk >> 3) * 4 + (c >> 5)) * 512 + ((kk & 7) * 32 + (c & 31)) * 2; }
; __device__ __forceinline__ int v_rd_base(int lane) { return ((lane & 3) << 3) | (((lane >> 2) & 3) << 6) | (((lane >> 4) & 1) << 5) | (((lane >> 5) & 1) << 8); }
; template <class TIn, class TOut, int QS, int KS, int OS, bool BIAS, bool PREF = true>
; __device__ __forceinline__ void causal_swa_block(const BlockRef<TIn, TOut>& cur, const BlockRef<TIn, TOut>& nxt, int skv, int W, char* lds, Seam<TIn>& S) {
;     ...
;     float m_reg = BIAS ? ((const float*)(lds + BIAS_OFF))[cur.P0 + wid * QBLK + r32] : -1e30f, l_reg = 0; f32x16 o[4] = {};
;     const int sr = tid >> 4, sc = (tid & 15) * 8, vst0 = v_st(sr, sc), vst1 = v_st(32 + sr, sc), kws = KSWZ(sr, sc * 2);
;     const int vb0 = (int)(uintptr_t)V_lds + v_rd_base(lane);
;     const TIn* Kh = cur.K; const TIn* Vh = cur.V;
;     const float* bias0 = (const float*)(lds + BIAS_OFF) + 4 * hi;
;     ...
;     constexpr int NQL = F32 ? 16 : 8;
;     constexpr bool SK = WSKIP && !F32;
;     ...
;     f32x16 pA0, pA1, pB0, pB1; float mnA, mnB, alA, alB; bf16x8 pa0, pa1, pa2, pa3;
.LBB0_639:
	v_exp_f32_e32 v164, v21
	v_sub_f32_e32 v21, v35, v36
	v_mul_f32_e32 v21, 0x3e0293ee, v21
	v_exp_f32_e32 v21, v21
	v_exp_f32_e32 v163, v37
	v_exp_f32_e32 v165, v38
	v_exp_f32_e32 v129, v39
	v_cndmask_b32_e64 v220, v21, 1.0, s[0:1]
	s_and_b32 s0, s19, 0x3fffffc0
	v_exp_f32_e32 v128, v22
	v_exp_f32_e32 v162, v23
	v_exp_f32_e32 v126, v24
	v_exp_f32_e32 v127, v25
	v_exp_f32_e32 v121, v26
	v_exp_f32_e32 v124, v27
	v_exp_f32_e32 v119, v28
	v_exp_f32_e32 v122, v29
	v_exp_f32_e32 v118, v30
	v_exp_f32_e32 v125, v18
	v_exp_f32_e32 v120, v19
	v_exp_f32_e32 v123, v20
	s_lshl_b32 s0, s0, 2
	s_add_i32 s0, s0, 0
	s_add_i32 s0, s0, 0x10000
	v_pk_fma_f32 v[112:113], v[16:17], s[22:23], v[34:35] op_sel_hi:[1,0,0]
	v_pk_fma_f32 v[110:111], v[14:15], s[22:23], v[34:35] op_sel_hi:[1,0,0]
	v_pk_fma_f32 v[108:109], v[12:13], s[22:23], v[34:35] op_sel_hi:[1,0,0]
	v_pk_fma_f32 v[106:107], v[10:11], s[22:23], v[34:35] op_sel_hi:[1,0,0]
	v_pk_fma_f32 v[104:105], v[8:9], s[22:23], v[34:35] op_sel_hi:[1,0,0]
	v_pk_fma_f32 v[102:103], v[6:7], s[22:23], v[34:35] op_sel_hi:[1,0,0]
	v_pk_fma_f32 v[114:115], v[4:5], s[22:23], v[34:35] op_sel_hi:[1,0,0]
	v_pk_fma_f32 v[116:117], v[2:3], s[22:23], v[34:35] op_sel_hi:[1,0,0]
	s_mov_b32 s17, 2
	s_cmp_lt_i32 s31, 3
	v_lshl_add_u32 v218, v216, 2, s0
	v_lshl_add_u32 v201, v217, 2, s0
	s_waitcnt lgkmcnt(0)
	s_barrier
	s_cbranch_scc1 .LBB0_658
	v_add_u32_e32 v2, s30, v216
	v_subrev_u32_e32 v2, s18, v2
	s_lshl_b32 s0, s18, 2
	v_sub_u32_e32 v2, v2, v217
	s_add_i32 s22, s18, 0x7f
	s_add_i32 s0, s0, 0
	v_add_u32_e32 v217, 0xffffff45, v2
	v_add_u32_e32 v2, s0, v196
	s_add_u32 s0, s6, s20
	s_addc_u32 s1, s7, s21
	s_add_u32 s0, s0, s10
	s_addc_u32 s1, s1, s11
	v_mov_b32_e32 v195, 0
	v_lshrrev_b32_e32 v254, 2, v0
	v_and_b32_e32 v254, 7, v254
	v_lshrrev_b32_e32 v255, 7, v0
	v_lshl_or_b32 v254, v255, 3, v254
	v_and_b32_e32 v253, 4, v254
	v_lshlrev_b32_e32 v253, 1, v253
	v_and_b32_e32 v255, 8, v254
	v_lshrrev_b32_e32 v255, 1, v255
	v_or_b32_e32 v253, v253, v255
	v_and_b32_e32 v254, 0x13, v254
	v_or_b32_e32 v254, v254, v253
	v_lshlrev_b32_e32 v254, 11, v254
	v_lshrrev_b32_e32 v253, 5, v0
	v_and_b32_e32 v253, 3, v253
	v_lshlrev_b32_e32 v253, 6, v253
	v_and_b32_e32 v255, 3, v0
	v_lshlrev_b32_e32 v255, 4, v255
	v_or3_b32 v254, v254, v253, v255
	v_lshrrev_b32_e32 v253, 4, v0
	v_and_b32_e32 v253, 7, v253
	v_lshlrev_b32_e32 v253, 4, v253
	v_xor_b32_e32 v253, v253, v194
	s_add_u32 s0, s72, s0
	v_add_u32_e32 v221, 0x10900, v2
	s_addc_u32 s1, s73, s1
	v_mov_b32_e32 v205, v195
	s_mov_b32 s20, 0x9640000
	s_mov_b32 s21, 0x7640000
	s_mov_b32 s26, 0x41000000
	s_mov_b32 s16, 0x3e0293ee
	v_mov_b32_e32 v222, 0xff800000
	v_mov_b32_e32 v216, v195
	v_mov_b32_e32 v50, v195
	v_mov_b32_e32 v51, v195
	v_mov_b32_e32 v52, v195
	v_mov_b32_e32 v53, v195
	v_mov_b32_e32 v54, v195
	v_mov_b32_e32 v55, v195
	v_mov_b32_e32 v56, v195
	v_mov_b32_e32 v57, v195
	v_mov_b32_e32 v58, v195
	v_mov_b32_e32 v59, v195
	v_mov_b32_e32 v60, v195
	v_mov_b32_e32 v61, v195
	v_mov_b32_e32 v62, v195
	v_mov_b32_e32 v63, v195
	v_mov_b32_e32 v64, v195
	v_mov_b32_e32 v65, v195
	v_mov_b32_e32 v34, v195
	v_mov_b32_e32 v35, v195
	v_mov_b32_e32 v36, v195
	v_mov_b32_e32 v37, v195
	v_mov_b32_e32 v38, v195
	v_mov_b32_e32 v39, v195
	v_mov_b32_e32 v40, v195
	v_mov_b32_e32 v41, v195
	v_mov_b32_e32 v42, v195
	v_mov_b32_e32 v43, v195
	v_mov_b32_e32 v44, v195
	v_mov_b32_e32 v45, v195
	v_mov_b32_e32 v46, v195
	v_mov_b32_e32 v47, v195
	v_mov_b32_e32 v48, v195
	v_mov_b32_e32 v49, v195
	v_mov_b32_e32 v18, v195
	v_mov_b32_e32 v19, v195
	v_mov_b32_e32 v20, v195
	v_mov_b32_e32 v21, v195
	v_mov_b32_e32 v22, v195
	v_mov_b32_e32 v23, v195
	v_mov_b32_e32 v24, v195
	v_mov_b32_e32 v25, v195
	v_mov_b32_e32 v26, v195
	v_mov_b32_e32 v27, v195
	v_mov_b32_e32 v28, v195
	v_mov_b32_e32 v29, v195
	v_mov_b32_e32 v30, v195
	v_mov_b32_e32 v31, v195
	v_mov_b32_e32 v32, v195
	v_mov_b32_e32 v33, v195
	v_mov_b32_e32 v2, v195
	v_mov_b32_e32 v3, v195
	v_mov_b32_e32 v4, v195
	v_mov_b32_e32 v5, v195
	v_mov_b32_e32 v6, v195
	v_mov_b32_e32 v7, v195
	v_mov_b32_e32 v8, v195
	v_mov_b32_e32 v9, v195
	v_mov_b32_e32 v10, v195
	v_mov_b32_e32 v11, v195
	v_mov_b32_e32 v12, v195
	v_mov_b32_e32 v13, v195
	v_mov_b32_e32 v14, v195
	v_mov_b32_e32 v15, v195
	v_mov_b32_e32 v16, v195
	v_mov_b32_e32 v17, v195
	s_branch .LBB0_643
.LBB0_641:
	s_or_b64 exec, exec, s[18:19]
	s_waitcnt lgkmcnt(0)
	ds_read_b128 v[168:171], v201 offset:224
	ds_read_b128 v[172:175], v201 offset:192
	ds_read_b128 v[176:179], v201 offset:160
	ds_read_b128 v[180:183], v201 offset:128
	s_waitcnt lgkmcnt(3)
	v_pk_mul_f32 v[64:65], v[64:65], v[170:171]
	s_waitcnt lgkmcnt(2)
	v_pk_mul_f32 v[60:61], v[60:61], v[174:175]
	s_waitcnt lgkmcnt(1)
	v_pk_mul_f32 v[56:57], v[56:57], v[178:179]
	s_waitcnt lgkmcnt(0)
	v_pk_mul_f32 v[52:53], v[52:53], v[182:183]
	v_pk_mul_f32 v[62:63], v[62:63], v[168:169]
	v_pk_mul_f32 v[58:59], v[58:59], v[172:173]
	v_pk_mul_f32 v[54:55], v[54:55], v[176:177]
	v_pk_mul_f32 v[50:51], v[50:51], v[180:181]
	v_pk_mul_f32 v[48:49], v[48:49], v[170:171]
	v_pk_mul_f32 v[44:45], v[44:45], v[174:175]
	v_pk_mul_f32 v[40:41], v[40:41], v[178:179]
	v_pk_mul_f32 v[36:37], v[36:37], v[182:183]
	v_pk_mul_f32 v[46:47], v[46:47], v[168:169]
	v_pk_mul_f32 v[42:43], v[42:43], v[172:173]
	v_pk_mul_f32 v[38:39], v[38:39], v[176:177]
	v_pk_mul_f32 v[34:35], v[34:35], v[180:181]
	v_pk_mul_f32 v[32:33], v[32:33], v[170:171]
	v_pk_mul_f32 v[28:29], v[28:29], v[174:175]
	v_pk_mul_f32 v[24:25], v[24:25], v[178:179]
	v_pk_mul_f32 v[20:21], v[20:21], v[182:183]
	v_pk_mul_f32 v[30:31], v[30:31], v[168:169]
	v_pk_mul_f32 v[26:27], v[26:27], v[172:173]
	v_pk_mul_f32 v[22:23], v[22:23], v[176:177]
	v_pk_mul_f32 v[18:19], v[18:19], v[180:181]
	v_pk_mul_f32 v[16:17], v[16:17], v[170:171]
	v_pk_mul_f32 v[12:13], v[12:13], v[174:175]
	v_pk_mul_f32 v[8:9], v[8:9], v[178:179]
	v_pk_mul_f32 v[4:5], v[4:5], v[182:183]
	v_pk_mul_f32 v[14:15], v[14:15], v[168:169]
	v_pk_mul_f32 v[10:11], v[10:11], v[172:173]
	v_pk_mul_f32 v[6:7], v[6:7], v[176:177]
	v_pk_mul_f32 v[2:3], v[2:3], v[180:181]
; template <int KB, bool SK, bool BIAS>
; __device__ __forceinline__ void qkt(f32x16& p0, f32x16& p1, const char* K_lds, int r32, int hi, const bf16x8* qr, bool act, const float* bl) {
;     ...
;     const char* kb[4];
; #pragma unroll
;     for (int dd = 0; dd < 4; ++dd) kb[dd] = K_lds + KB * SHM_K + KSWZ(r32, (dd * 16 + hi * 8) * 2);
; #pragma unroll
;     for (int d0 = 0; d0 < 8; ++d0) { const char* a = kb[d0 & 3] + (d0 >> 2) * 128;
;         bf16x8 b0 = *reinterpret_cast<const bf16x8*>(a);
;         bf16x8 b1 = *reinterpret_cast<const bf16x8*>(a + 32 * 256);
;         p0 = __builtin_amdgcn_mfma_f32_32x32x16_bf16(b0, qr[d0], p0, 0, 0, 0);
;         p1 = __builtin_amdgcn_mfma_f32_32x32x16_bf16(b1, qr[d0], p1, 0, 0, 0); }
.LBB0_642:
	v_cndmask_b32_e64 v178, v162, v226, s[6:7]
	v_mul_f32_e32 v168, 0xbe0293ee, v178
	v_mov_b32_e32 v172, v168
	v_fmamk_f32 v114, v114, 0x3e0293ee, v168
	v_fmamk_f32 v115, v115, 0x3e0293ee, v168
	v_fmamk_f32 v116, v116, 0x3e0293ee, v168
	v_fmamk_f32 v117, v117, 0x3e0293ee, v168
	v_fmamk_f32 v118, v118, 0x3e0293ee, v168
	v_fmamk_f32 v119, v119, 0x3e0293ee, v168
	v_fmamk_f32 v120, v120, 0x3e0293ee, v168
	v_fmamk_f32 v121, v121, 0x3e0293ee, v168
	v_fmamk_f32 v122, v122, 0x3e0293ee, v168
	v_fmamk_f32 v123, v123, 0x3e0293ee, v168
	v_fmamk_f32 v167, v124, 0x3e0293ee, v168
	v_fmamk_f32 v125, v125, 0x3e0293ee, v168
	v_fmamk_f32 v169, v126, 0x3e0293ee, v168
	v_fmamk_f32 v170, v127, 0x3e0293ee, v168
	v_fmamk_f32 v171, v128, 0x3e0293ee, v168
	v_fmac_f32_e32 v172, 0x3e0293ee, v129
	v_exp_f32_e32 v163, v114
	v_exp_f32_e32 v165, v115
	v_exp_f32_e32 v129, v116
	v_exp_f32_e32 v164, v117
	v_exp_f32_e32 v128, v118
	v_exp_f32_e32 v162, v119
	v_exp_f32_e32 v126, v120
	v_exp_f32_e32 v127, v121
	v_exp_f32_e32 v121, v122
	v_exp_f32_e32 v124, v123
	v_exp_f32_e32 v119, v167
	v_exp_f32_e32 v122, v125
	v_exp_f32_e32 v118, v169
	v_exp_f32_e32 v125, v170
	v_exp_f32_e32 v120, v171
	v_exp_f32_e32 v123, v172
	s_addk_i32 s22, 0x80
	v_pk_fma_f32 v[116:117], v[98:99], s[16:17], v[168:169] op_sel_hi:[1,0,0]
	v_add_f32_e32 v98, v223, v224
	s_add_u32 s0, s0, 0x40000
	v_pk_fma_f32 v[112:113], v[112:113], s[16:17], v[168:169] op_sel_hi:[1,0,0]
	v_pk_fma_f32 v[110:111], v[110:111], s[16:17], v[168:169] op_sel_hi:[1,0,0]
	v_pk_fma_f32 v[108:109], v[108:109], s[16:17], v[168:169] op_sel_hi:[1,0,0]
	v_pk_fma_f32 v[106:107], v[106:107], s[16:17], v[168:169] op_sel_hi:[1,0,0]
	v_pk_fma_f32 v[104:105], v[104:105], s[16:17], v[168:169] op_sel_hi:[1,0,0]
	v_pk_fma_f32 v[102:103], v[102:103], s[16:17], v[168:169] op_sel_hi:[1,0,0]
	v_pk_fma_f32 v[114:115], v[100:101], s[16:17], v[168:169] op_sel_hi:[1,0,0]
	v_fmac_f32_e32 v98, v220, v216
	v_add_f32_e32 v216, v227, v228
	s_addc_u32 s1, s1, 0
	s_add_i32 s17, s17, 2
	v_fmac_f32_e32 v216, v98, v225
	v_add_u32_e32 v217, 0xffffff80, v217
	s_cmp_ge_i32 s17, s31
	v_add_u32_e32 v221, 0x200, v221
	v_mov_b32_e32 v220, v166
	s_waitcnt lgkmcnt(0)
	s_barrier
	s_cbranch_scc1 .LBB0_659
.LBB0_643:
	s_add_u32 s98, s0, 0x7640000
	s_addc_u32 s99, s1, 0
	s_lshl_b32 s100, s75, 10
	s_add_i32 m0, s100, 0x8000
	s_nop 0
	global_load_lds_dwordx4 v253, s[98:99]
	s_add_u32 s98, s98, 0x10000
	s_addc_u32 s99, s99, 0
	s_add_i32 m0, m0, 0x2000
	s_nop 0
	global_load_lds_dwordx4 v253, s[98:99]
	ds_read_b128 v[66:69], v208 offset:49152
	ds_read_b128 v[86:89], v221
	ds_read_b128 v[90:93], v221 offset:32
	ds_read_b128 v[94:97], v221 offset:64
	ds_read_b128 v[98:101], v221 offset:96
	ds_read_b128 v[166:169], v208 offset:57344
	ds_read_b128 v[170:173], v208 offset:49280
	v_exp_f32_e32 v179, v102
	v_add_f32_e32 v102, 0, v163
	s_waitcnt lgkmcnt(2)
	v_mfma_f32_32x32x16_bf16 v[86:101], v[66:69], v[158:161], v[86:101]
	ds_read_b128 v[70:73], v221 offset:128
	ds_read_b128 v[74:77], v221 offset:160
	ds_read_b128 v[78:81], v221 offset:192
	ds_read_b128 v[82:85], v221 offset:224
	ds_read_b128 v[66:69], v208 offset:57472
	v_add_f32_e32 v102, v165, v102
	v_add_f32_e32 v102, v129, v102
	v_add_f32_e32 v102, v164, v102
	v_add_f32_e32 v102, v128, v102
	v_add_f32_e32 v102, v162, v102
	v_add_f32_e32 v102, v126, v102
	s_waitcnt lgkmcnt(1)
	v_mfma_f32_32x32x16_bf16 v[70:85], v[166:169], v[158:161], v[70:85]
	ds_read_b128 v[166:169], v209 offset:49152
	ds_read_b128 v[174:177], v209 offset:57344
	ds_read_b128 v[180:183], v209 offset:49280
	v_add_f32_e32 v102, v127, v102
	v_add_f32_e32 v102, v121, v102
	v_add_f32_e32 v102, v124, v102
	v_add_f32_e32 v102, v119, v102
	v_add_f32_e32 v102, v122, v102
	s_waitcnt lgkmcnt(2)
	v_mfma_f32_32x32x16_bf16 v[86:101], v[166:169], v[154:157], v[86:101]
	ds_read_b128 v[166:169], v209 offset:57472
	ds_read_b128 v[184:187], v211 offset:49152
	ds_read_b128 v[188:191], v211 offset:49280
	ds_read_b128 v[224:227], v211 offset:57344
	ds_read_b128 v[228:231], v211 offset:57472
	ds_read_b128 v[232:235], v212 offset:49152
	ds_read_b128 v[236:239], v212 offset:49280
	v_exp_f32_e32 v116, v116
	v_add_f32_e32 v102, v118, v102
	v_exp_f32_e32 v117, v117
	v_add_f32_e32 v102, v125, v102
	v_exp_f32_e32 v114, v114
	v_add_f32_e32 v102, v120, v102
	s_waitcnt lgkmcnt(8)
	v_mfma_f32_32x32x16_bf16 v[70:85], v[174:177], v[154:157], v[70:85]
	ds_read_b128 v[174:177], v212 offset:57344
	ds_read_b128 v[240:243], v212 offset:57472
	v_exp_f32_e32 v115, v115
	v_add_f32_e32 v102, v123, v102
	v_add_f32_e32 v102, v116, v102
	v_add_f32_e32 v102, v117, v102
	v_add_f32_e32 v102, v114, v102
	v_add_f32_e32 v102, v115, v102
	s_waitcnt lgkmcnt(7)
	v_mfma_f32_32x32x16_bf16 v[86:101], v[184:187], v[150:153], v[86:101]
	v_exp_f32_e32 v184, v103
	v_exp_f32_e32 v185, v104
	v_exp_f32_e32 v186, v105
	v_exp_f32_e32 v187, v106
	v_add_f32_e32 v102, v179, v102
	v_exp_f32_e32 v192, v107
	v_add_f32_e32 v102, v184, v102
	s_waitcnt lgkmcnt(5)
	v_mfma_f32_32x32x16_bf16 v[70:85], v[224:227], v[150:153], v[70:85]
	v_exp_f32_e32 v193, v108
	v_add_f32_e32 v102, v185, v102
	v_exp_f32_e32 v196, v109
	v_add_f32_e32 v102, v186, v102
	v_exp_f32_e32 v197, v110
	v_exp_f32_e32 v206, v111
	v_exp_f32_e32 v207, v112
	s_waitcnt lgkmcnt(3)
	v_mfma_f32_32x32x16_bf16 v[86:101], v[232:235], v[146:149], v[86:101]
	v_exp_f32_e32 v113, v113
	s_sub_i32 s6, s22, 63
	s_waitcnt lgkmcnt(1)
; __device__ __forceinline__ void finishSM(f32x16& p0, f32x16& p1, float alpha, float& l_reg, bf16x8& pa0, bf16x8& pa1, bf16x8& pa2, bf16x8& pa3) {
;     for (int r = 0; r < 16; ++r) p1[r] = __builtin_amdgcn_exp2f(p1[r]);
;     float ps = 0; for (int r = 0; r < 16; ++r) ps += p0[r]; for (int r = 0; r < 16; ++r) ps += p1[r];
;     { auto rr = __builtin_amdgcn_permlane32_swap(__float_as_uint(ps), __float_as_uint(ps), false, false);
;       ps = __uint_as_float(rr[0]) + __uint_as_float(rr[1]); }
;     l_reg = l_reg * alpha + ps;
;     ...
;     PK4(p0, 0, pa0); PK4(p0, 8, pa1); PK4(p1, 0, pa2); PK4(p1, 8, pa3);
;     ...
; }
; template <int VB, bool SK>
; __device__ __forceinline__ void pv_tile(f32x16* o, int vb0, bf16x8 pa0, bf16x8 pa1, bf16x8 pa2, bf16x8 pa3, bool act) {
;     if (SK && !act) return;
;     ...
;     PV_D0(0); PV_D0(1); PV_D0(2); PV_D0(3);
	v_mfma_f32_32x32x16_bf16 v[70:85], v[174:177], v[146:149], v[70:85]
	v_mfma_f32_32x32x16_bf16 v[86:101], v[170:173], v[142:145], v[86:101]
	v_mfma_f32_32x32x16_bf16 v[70:85], v[66:69], v[142:145], v[70:85]
	v_add_f32_e32 v66, v187, v102
	v_add_f32_e32 v66, v192, v66
	v_add_f32_e32 v66, v193, v66
	v_add_f32_e32 v66, v196, v66
	v_add_f32_e32 v66, v197, v66
	v_add_f32_e32 v66, v206, v66
	v_add_f32_e32 v66, v207, v66
	v_mfma_f32_32x32x16_bf16 v[86:101], v[180:183], v[138:141], v[86:101]
	v_add_f32_e32 v223, v113, v66
	v_mov_b32_e32 v224, v223
	s_nop 1
	v_permlane32_swap_b32_e32 v223, v224
	v_cvt_pk_bf16_f32 v66, v163, v165
	v_cvt_pk_bf16_f32 v67, v129, v164
	v_cvt_pk_bf16_f32 v68, v128, v162
	v_mfma_f32_32x32x16_bf16 v[70:85], v[166:169], v[138:141], v[70:85]
	v_cvt_pk_bf16_f32 v69, v126, v127
	v_cvt_pk_bf16_f32 v102, v121, v124
	v_cvt_pk_bf16_f32 v103, v119, v122
	v_cvt_pk_bf16_f32 v104, v118, v125
	v_cvt_pk_bf16_f32 v105, v120, v123
	v_cvt_pk_bf16_f32 v106, v116, v117
	v_cvt_pk_bf16_f32 v107, v114, v115
	v_mfma_f32_32x32x16_bf16 v[86:101], v[188:191], v[134:137], v[86:101]
	v_cvt_pk_bf16_f32 v108, v179, v184
	v_cvt_pk_bf16_f32 v109, v185, v186
	v_cvt_pk_bf16_f32 v110, v187, v192
	v_cvt_pk_bf16_f32 v111, v193, v196
	v_cvt_pk_bf16_f32 v112, v197, v206
	v_cvt_pk_bf16_f32 v113, v207, v113
	v_permlane32_swap_b32_e32 v66, v68
	v_mfma_f32_32x32x16_bf16 v[70:85], v[228:231], v[134:137], v[70:85]
	v_permlane32_swap_b32_e32 v67, v69
	v_permlane32_swap_b32_e32 v102, v104
	v_permlane32_swap_b32_e32 v103, v105
	v_permlane32_swap_b32_e32 v106, v108
	v_mfma_f32_32x32x16_bf16 v[86:101], v[236:239], v[130:133], v[86:101]
	v_permlane32_swap_b32_e32 v107, v109
	v_permlane32_swap_b32_e32 v110, v112
	v_permlane32_swap_b32_e32 v111, v113
	s_waitcnt lgkmcnt(0)
	v_mfma_f32_32x32x16_bf16 v[70:85], v[240:243], v[130:133], v[70:85]
	ds_read_b64_tr_b16 v[114:115], v199 offset:0
	ds_read_b64_tr_b16 v[116:117], v199 offset:0x800
	ds_read_b64_tr_b16 v[118:119], v199 offset:0x1000
	ds_read_b64_tr_b16 v[120:121], v199 offset:0x1800
	ds_read_b64_tr_b16 v[122:123], v199 offset:0x2000
	ds_read_b64_tr_b16 v[124:125], v199 offset:0x2800
	ds_read_b64_tr_b16 v[126:127], v199 offset:0x3000
	ds_read_b64_tr_b16 v[128:129], v199 offset:0x3800
	s_waitcnt lgkmcnt(0)
	s_nop 0
	v_mfma_f32_32x32x16_bf16 v[50:65], v[66:69], v[114:117], v[50:65]
	ds_read_b64_tr_b16 v[114:115], v199 offset:0x200
	ds_read_b64_tr_b16 v[116:117], v199 offset:0xa00
	v_mfma_f32_32x32x16_bf16 v[50:65], v[102:105], v[118:121], v[50:65]
	ds_read_b64_tr_b16 v[118:119], v199 offset:0x1200
	ds_read_b64_tr_b16 v[120:121], v199 offset:0x1a00
	v_mfma_f32_32x32x16_bf16 v[50:65], v[106:109], v[122:125], v[50:65]
	ds_read_b64_tr_b16 v[122:123], v199 offset:0x2200
	ds_read_b64_tr_b16 v[124:125], v199 offset:0x2a00
	ds_read_b64_tr_b16 v[180:181], v199 offset:0x3200
	ds_read_b64_tr_b16 v[182:183], v199 offset:0x3a00
	s_waitcnt lgkmcnt(0)
	v_mfma_f32_32x32x16_bf16 v[50:65], v[110:113], v[126:129], v[50:65]
	v_mfma_f32_32x32x16_bf16 v[34:49], v[66:69], v[114:117], v[34:49]
	ds_read_b64_tr_b16 v[114:115], v199 offset:0x400
	ds_read_b64_tr_b16 v[116:117], v199 offset:0xc00
	v_mfma_f32_32x32x16_bf16 v[34:49], v[102:105], v[118:121], v[34:49]
	ds_read_b64_tr_b16 v[118:119], v199 offset:0x1400
	ds_read_b64_tr_b16 v[120:121], v199 offset:0x1c00
	v_mfma_f32_32x32x16_bf16 v[34:49], v[106:109], v[122:125], v[34:49]
	ds_read_b64_tr_b16 v[122:123], v199 offset:0x2400
	ds_read_b64_tr_b16 v[124:125], v199 offset:0x2c00
	ds_read_b64_tr_b16 v[126:127], v199 offset:0x3400
	ds_read_b64_tr_b16 v[128:129], v199 offset:0x3c00
	s_waitcnt lgkmcnt(0)
	v_mfma_f32_32x32x16_bf16 v[34:49], v[110:113], v[180:183], v[34:49]
	v_mfma_f32_32x32x16_bf16 v[18:33], v[66:69], v[114:117], v[18:33]
	ds_read_b64_tr_b16 v[114:115], v199 offset:0x600
	ds_read_b64_tr_b16 v[116:117], v199 offset:0xe00
	v_mfma_f32_32x32x16_bf16 v[18:33], v[102:105], v[118:121], v[18:33]
	ds_read_b64_tr_b16 v[118:119], v199 offset:0x1600
	ds_read_b64_tr_b16 v[120:121], v199 offset:0x1e00
	v_mfma_f32_32x32x16_bf16 v[18:33], v[106:109], v[122:125], v[18:33]
	ds_read_b64_tr_b16 v[122:123], v199 offset:0x2600
	ds_read_b64_tr_b16 v[124:125], v199 offset:0x2e00
	ds_read_b64_tr_b16 v[180:181], v199 offset:0x3600
	ds_read_b64_tr_b16 v[182:183], v199 offset:0x3e00
	s_waitcnt lgkmcnt(0)
	v_mfma_f32_32x32x16_bf16 v[18:33], v[110:113], v[126:129], v[18:33]
	v_mfma_f32_32x32x16_bf16 v[2:17], v[66:69], v[114:117], v[2:17]
	s_cmp_le_u32 s22, s30
	s_cselect_b64 s[18:19], -1, 0
	s_cmp_gt_i32 s6, s25
	s_cselect_b64 s[6:7], -1, 0
	s_and_b64 s[6:7], s[6:7], s[18:19]
	s_and_b64 vcc, exec, s[6:7]
	v_mfma_f32_32x32x16_bf16 v[2:17], v[102:105], v[118:121], v[2:17]
	v_mfma_f32_32x32x16_bf16 v[2:17], v[106:109], v[122:125], v[2:17]
	v_mfma_f32_32x32x16_bf16 v[2:17], v[110:113], v[180:183], v[2:17]
	s_cbranch_vccnz .LBB0_645
; __device__ __forceinline__ void mask_tile(f32x16& p0, f32x16& p1, int dq, unsigned W) {
;     const float NEG = -__builtin_inff();
; #pragma unroll
;     for (int r = 0; r < 16; ++r) {
;         const int c = (r & 3) + 8 * (r >> 2);
;         if ((unsigned)(dq - c) >= W) p0[r] = NEG;
;         if ((unsigned)(dq - c - 32) >= W) p1[r] = NEG;
;     }
; }
; __device__ __forceinline__ void partialSM(f32x16& p0, f32x16& p1, float& m_reg, float& mn, float& alpha) {
;     float pmax = p0[0]; for (int r = 1; r < 16; ++r) pmax = fmaxf(pmax, p0[r]); for (int r = 0; r < 16; ++r) pmax = fmaxf(pmax, p1[r]);
;     { auto rr = __builtin_amdgcn_permlane32_swap(__float_as_uint(pmax), __float_as_uint(pmax), false, false);
;       pmax = fmaxf(__uint_as_float(rr[0]), __uint_as_float(rr[1])); }
;     constexpr float C2 = 1.4426950408889634f * SCALE;
;     if (__builtin_expect(__all((pmax - m_reg) * SCALE <= THR), 1)) { mn = m_reg; alpha = 1.f; }
;     else { mn = fmaxf(m_reg, pmax); alpha = __builtin_amdgcn_exp2f((m_reg - mn) * C2); m_reg = mn; }
	v_add_u32_e32 v66, 0x7b, v217
	v_cmp_gt_u32_e32 vcc, s24, v66
	v_add_u32_e32 v66, 0x5b, v217
	s_nop 0
	v_cndmask_b32_e32 v86, v222, v86, vcc
	v_cmp_gt_u32_e32 vcc, s24, v66
	v_add_u32_e32 v66, 0x7a, v217
	s_nop 0
	v_cndmask_b32_e32 v70, v222, v70, vcc
	v_cmp_gt_u32_e32 vcc, s24, v66
	v_add_u32_e32 v66, 0x5a, v217
	s_nop 0
	v_cndmask_b32_e32 v87, v222, v87, vcc
	v_cmp_gt_u32_e32 vcc, s24, v66
	v_add_u32_e32 v66, 0x79, v217
	s_nop 0
	v_cndmask_b32_e32 v71, v222, v71, vcc
	v_cmp_gt_u32_e32 vcc, s24, v66
	v_add_u32_e32 v66, 0x59, v217
	s_nop 0
	v_cndmask_b32_e32 v88, v222, v88, vcc
	v_cmp_gt_u32_e32 vcc, s24, v66
	v_add_u32_e32 v66, 0x78, v217
	s_nop 0
	v_cndmask_b32_e32 v72, v222, v72, vcc
	v_cmp_gt_u32_e32 vcc, s24, v66
	v_add_u32_e32 v66, 0x58, v217
	s_nop 0
	v_cndmask_b32_e32 v89, v222, v89, vcc
	v_cmp_gt_u32_e32 vcc, s24, v66
	v_add_u32_e32 v66, 0x73, v217
	s_nop 0
	v_cndmask_b32_e32 v73, v222, v73, vcc
	v_cmp_gt_u32_e32 vcc, s24, v66
	v_add_u32_e32 v66, 0x53, v217
	s_nop 0
	v_cndmask_b32_e32 v90, v222, v90, vcc
	v_cmp_gt_u32_e32 vcc, s24, v66
	v_add_u32_e32 v66, 0x72, v217
	s_nop 0
	v_cndmask_b32_e32 v74, v222, v74, vcc
	v_cmp_gt_u32_e32 vcc, s24, v66
	v_add_u32_e32 v66, 0x52, v217
	s_nop 0
	v_cndmask_b32_e32 v91, v222, v91, vcc
	v_cmp_gt_u32_e32 vcc, s24, v66
	v_add_u32_e32 v66, 0x71, v217
	s_nop 0
	v_cndmask_b32_e32 v75, v222, v75, vcc
	v_cmp_gt_u32_e32 vcc, s24, v66
	v_add_u32_e32 v66, 0x51, v217
	s_nop 0
	v_cndmask_b32_e32 v92, v222, v92, vcc
	v_cmp_gt_u32_e32 vcc, s24, v66
	v_add_u32_e32 v66, 0x70, v217
	s_nop 0
	v_cndmask_b32_e32 v76, v222, v76, vcc
	v_cmp_gt_u32_e32 vcc, s24, v66
	v_add_u32_e32 v66, 0x50, v217
	s_nop 0
	v_cndmask_b32_e32 v93, v222, v93, vcc
	v_cmp_gt_u32_e32 vcc, s24, v66
	v_add_u32_e32 v66, 0x6b, v217
	s_nop 0
	v_cndmask_b32_e32 v77, v222, v77, vcc
	v_cmp_gt_u32_e32 vcc, s24, v66
	v_add_u32_e32 v66, 0x4b, v217
	s_nop 0
	v_cndmask_b32_e32 v94, v222, v94, vcc
	v_cmp_gt_u32_e32 vcc, s24, v66
	v_add_u32_e32 v66, 0x6a, v217
	s_nop 0
	v_cndmask_b32_e32 v78, v222, v78, vcc
	v_cmp_gt_u32_e32 vcc, s24, v66
	v_add_u32_e32 v66, 0x4a, v217
	s_nop 0
	v_cndmask_b32_e32 v95, v222, v95, vcc
	v_cmp_gt_u32_e32 vcc, s24, v66
	v_add_u32_e32 v66, 0x69, v217
	s_nop 0
	v_cndmask_b32_e32 v79, v222, v79, vcc
	v_cmp_gt_u32_e32 vcc, s24, v66
	v_add_u32_e32 v66, 0x49, v217
	s_nop 0
	v_cndmask_b32_e32 v96, v222, v96, vcc
	v_cmp_gt_u32_e32 vcc, s24, v66
	v_add_u32_e32 v66, 0x68, v217
	s_nop 0
	v_cndmask_b32_e32 v80, v222, v80, vcc
	v_cmp_gt_u32_e32 vcc, s24, v66
	v_add_u32_e32 v66, 0x48, v217
	s_nop 0
	v_cndmask_b32_e32 v97, v222, v97, vcc
	v_cmp_gt_u32_e32 vcc, s24, v66
	v_add_u32_e32 v66, 0x63, v217
	s_nop 0
	v_cndmask_b32_e32 v81, v222, v81, vcc
	v_cmp_gt_u32_e32 vcc, s24, v66
	v_add_u32_e32 v66, 0x43, v217
	s_nop 0
	v_cndmask_b32_e32 v98, v222, v98, vcc
	v_cmp_gt_u32_e32 vcc, s24, v66
	v_add_u32_e32 v66, 0x62, v217
	s_nop 0
	v_cndmask_b32_e32 v82, v222, v82, vcc
	v_cmp_gt_u32_e32 vcc, s24, v66
	v_add_u32_e32 v66, 0x42, v217
	s_nop 0
	v_cndmask_b32_e32 v99, v222, v99, vcc
	v_cmp_gt_u32_e32 vcc, s24, v66
	v_add_u32_e32 v66, 0x61, v217
	s_nop 0
	v_cndmask_b32_e32 v83, v222, v83, vcc
	v_cmp_gt_u32_e32 vcc, s24, v66
	v_add_u32_e32 v66, 0x41, v217
	s_nop 0
	v_cndmask_b32_e32 v100, v222, v100, vcc
	v_cmp_gt_u32_e32 vcc, s24, v66
	v_add_u32_e32 v66, 0x60, v217
	s_nop 0
	v_cndmask_b32_e32 v84, v222, v84, vcc
	v_cmp_gt_u32_e32 vcc, s24, v66
	v_add_u32_e32 v66, 64, v217
	s_nop 0
	v_cndmask_b32_e32 v101, v222, v101, vcc
	v_cmp_gt_u32_e32 vcc, s24, v66
	s_nop 1
	v_cndmask_b32_e32 v85, v222, v85, vcc
.LBB0_645:
	v_max_f32_e32 v66, v87, v87
	v_max_f32_e32 v67, v86, v86
	v_max_f32_e32 v66, v67, v66
	v_max3_f32 v66, v66, v88, v89
	v_max3_f32 v66, v66, v90, v91
	v_max3_f32 v66, v66, v92, v93
	v_max3_f32 v66, v66, v94, v95
	v_max3_f32 v66, v66, v96, v97
	v_max3_f32 v66, v66, v98, v99
	v_max3_f32 v66, v66, v100, v101
	v_max3_f32 v66, v66, v70, v71
	v_max3_f32 v66, v66, v72, v73
	v_max3_f32 v66, v66, v74, v75
	v_max3_f32 v66, v66, v76, v77
	v_max3_f32 v66, v66, v78, v79
	v_max3_f32 v66, v66, v80, v81
	v_max3_f32 v66, v66, v82, v83
	v_max3_f32 v66, v66, v84, v85
	v_mov_b32_e32 v67, v66
	s_nop 1
	v_permlane32_swap_b32_e32 v66, v67
	v_max_f32_e32 v67, v67, v67
	v_max_f32_e32 v66, v66, v66
	v_max_f32_e32 v66, v66, v67
	v_max_f32_e32 v68, v178, v178
	v_sub_f32_e32 v67, v66, v178
	v_max_f32_e32 v66, v68, v66
	v_sub_f32_e32 v68, v178, v66
	v_mul_f32_e32 v68, 0x3e0293ee, v68
	v_mul_f32_e32 v67, 0x3db504f3, v67
	v_exp_f32_e32 v68, v68
	v_cmp_ge_f32_e32 vcc, s26, v67
	s_cmp_eq_u64 vcc, exec
	s_cselect_b64 s[6:7], -1, 0
	s_barrier
	v_cndmask_b32_e64 v225, v68, 1.0, s[6:7]
	v_cmp_gt_f32_e32 vcc, 1.0, v225
	s_add_u32 s98, s0, 0x9640000
	s_addc_u32 s99, s1, 0
	s_lshl_b32 s100, s75, 10
	s_add_i32 m0, s100, 0x0
	s_nop 0
	global_load_lds_dwordx4 v254, s[98:99]
	s_add_u32 s98, s98, 0x10000
	s_addc_u32 s99, s99, 0
	s_add_i32 m0, m0, 0x2000
	s_nop 0
	global_load_lds_dwordx4 v254, s[98:99]
	s_waitcnt vmcnt(2)
	s_cbranch_vccz .LBB0_649
	s_and_saveexec_b64 s[18:19], s[4:5]
	ds_write_b32 v218, v225 offset:128
	s_or_b64 exec, exec, s[18:19]
	s_waitcnt lgkmcnt(0)
	ds_read_b128 v[102:105], v201 offset:224
	ds_read_b128 v[106:109], v201 offset:192
	ds_read_b128 v[110:113], v201 offset:160
	ds_read_b128 v[114:117], v201 offset:128
	s_waitcnt lgkmcnt(3)
	v_pk_mul_f32 v[64:65], v[64:65], v[104:105]
	s_waitcnt lgkmcnt(2)
	v_pk_mul_f32 v[60:61], v[60:61], v[108:109]
	s_waitcnt lgkmcnt(1)
	v_pk_mul_f32 v[56:57], v[56:57], v[112:113]
	s_waitcnt lgkmcnt(0)
	v_pk_mul_f32 v[52:53], v[52:53], v[116:117]
	v_pk_mul_f32 v[62:63], v[62:63], v[102:103]
	v_pk_mul_f32 v[58:59], v[58:59], v[106:107]
	v_pk_mul_f32 v[54:55], v[54:55], v[110:111]
	v_pk_mul_f32 v[50:51], v[50:51], v[114:115]
	v_pk_mul_f32 v[48:49], v[48:49], v[104:105]
	v_pk_mul_f32 v[44:45], v[44:45], v[108:109]
	v_pk_mul_f32 v[40:41], v[40:41], v[112:113]
	v_pk_mul_f32 v[36:37], v[36:37], v[116:117]
	v_pk_mul_f32 v[46:47], v[46:47], v[102:103]
	v_pk_mul_f32 v[42:43], v[42:43], v[106:107]
	v_pk_mul_f32 v[38:39], v[38:39], v[110:111]
	v_pk_mul_f32 v[34:35], v[34:35], v[114:115]
	v_pk_mul_f32 v[32:33], v[32:33], v[104:105]
	v_pk_mul_f32 v[28:29], v[28:29], v[108:109]
	v_pk_mul_f32 v[24:25], v[24:25], v[112:113]
	v_pk_mul_f32 v[20:21], v[20:21], v[116:117]
	v_pk_mul_f32 v[30:31], v[30:31], v[102:103]
	v_pk_mul_f32 v[26:27], v[26:27], v[106:107]
	v_pk_mul_f32 v[22:23], v[22:23], v[110:111]
	v_pk_mul_f32 v[18:19], v[18:19], v[114:115]
	v_pk_mul_f32 v[16:17], v[16:17], v[104:105]
	v_pk_mul_f32 v[12:13], v[12:13], v[108:109]
	v_pk_mul_f32 v[8:9], v[8:9], v[112:113]
	v_pk_mul_f32 v[4:5], v[4:5], v[116:117]
	v_pk_mul_f32 v[14:15], v[14:15], v[102:103]
	v_pk_mul_f32 v[10:11], v[10:11], v[106:107]
	v_pk_mul_f32 v[6:7], v[6:7], v[110:111]
	v_pk_mul_f32 v[2:3], v[2:3], v[114:115]
; __device__ __forceinline__ void partialSM(f32x16& p0, f32x16& p1, float& m_reg, float& mn, float& alpha) {
;     ...
;     constexpr float C2 = 1.4426950408889634f * SCALE;
;     if (__builtin_expect(__all((pmax - m_reg) * SCALE <= THR), 1)) { mn = m_reg; alpha = 1.f; }
;     else { mn = fmaxf(m_reg, pmax); alpha = __builtin_amdgcn_exp2f((m_reg - mn) * C2); m_reg = mn; }
;     const float mnL = -mn * C2;
;     for (int r = 0; r < 16; ++r) p0[r] = fmaf(p0[r], C2, mnL); for (int r = 0; r < 16; ++r) p1[r] = fmaf(p1[r], C2, mnL);
;     for (int r = 0; r < 16; ++r) p0[r] = __builtin_amdgcn_exp2f(p0[r]);
.LBB0_649:
	v_cndmask_b32_e64 v226, v66, v178, s[6:7]
	v_mul_f32_e32 v178, 0xbe0293ee, v226
	v_fmamk_f32 v66, v86, 0x3e0293ee, v178
	v_fmamk_f32 v67, v87, 0x3e0293ee, v178
	v_fmamk_f32 v68, v88, 0x3e0293ee, v178
	v_fmamk_f32 v69, v89, 0x3e0293ee, v178
	v_fmamk_f32 v102, v90, 0x3e0293ee, v178
	v_fmamk_f32 v103, v91, 0x3e0293ee, v178
	v_fmamk_f32 v104, v92, 0x3e0293ee, v178
	v_fmamk_f32 v105, v93, 0x3e0293ee, v178
	v_fmamk_f32 v106, v94, 0x3e0293ee, v178
	v_fmamk_f32 v107, v95, 0x3e0293ee, v178
	v_fmamk_f32 v108, v96, 0x3e0293ee, v178
	v_fmamk_f32 v109, v97, 0x3e0293ee, v178
	v_fmamk_f32 v98, v98, 0x3e0293ee, v178
	v_fmamk_f32 v99, v99, 0x3e0293ee, v178
	v_fmamk_f32 v100, v100, 0x3e0293ee, v178
	v_fmamk_f32 v101, v101, 0x3e0293ee, v178
	v_fmamk_f32 v86, v70, 0x3e0293ee, v178
	v_fmamk_f32 v95, v71, 0x3e0293ee, v178
	v_fmamk_f32 v96, v72, 0x3e0293ee, v178
	v_fmamk_f32 v97, v73, 0x3e0293ee, v178
	v_fmamk_f32 v179, v74, 0x3e0293ee, v178
	v_fmamk_f32 v87, v75, 0x3e0293ee, v178
	v_fmamk_f32 v88, v76, 0x3e0293ee, v178
	v_fmamk_f32 v89, v77, 0x3e0293ee, v178
	v_fmamk_f32 v90, v78, 0x3e0293ee, v178
	v_fmamk_f32 v91, v79, 0x3e0293ee, v178
	v_fmamk_f32 v92, v80, 0x3e0293ee, v178
	v_fmamk_f32 v93, v81, 0x3e0293ee, v178
	v_exp_f32_e32 v66, v66
	v_exp_f32_e32 v67, v67
	v_exp_f32_e32 v68, v68
	v_exp_f32_e32 v69, v69
	v_exp_f32_e32 v70, v102
	v_exp_f32_e32 v71, v103
	v_exp_f32_e32 v72, v104
	v_exp_f32_e32 v73, v105
	v_exp_f32_e32 v74, v106
	v_exp_f32_e32 v75, v107
	v_exp_f32_e32 v76, v108
	v_exp_f32_e32 v77, v109
	v_exp_f32_e32 v78, v98
	v_exp_f32_e32 v79, v99
	v_exp_f32_e32 v80, v100
	v_exp_f32_e32 v81, v101
	v_fmamk_f32 v94, v82, 0x3e0293ee, v178
	v_fmamk_f32 v180, v83, 0x3e0293ee, v178
	v_fmamk_f32 v181, v84, 0x3e0293ee, v178
	v_fmac_f32_e32 v178, 0x3e0293ee, v85
	s_waitcnt lgkmcnt(0)
	s_barrier
	s_add_i32 s100, s17, 1
	s_cmp_lt_i32 s100, s31
	s_cbranch_scc0 .Lattn_k2skip_2
	s_add_u32 s98, s0, 0x7660000
	s_addc_u32 s99, s1, 0
	s_lshl_b32 s100, s75, 10
	s_add_i32 m0, s100, 0xc000
	s_nop 0
	global_load_lds_dwordx4 v253, s[98:99]
	s_add_u32 s98, s98, 0x10000
	s_addc_u32 s99, s99, 0
	s_add_i32 m0, m0, 0x2000
	s_nop 0
	global_load_lds_dwordx4 v253, s[98:99]
; __device__ __forceinline__ void finishSM(f32x16& p0, f32x16& p1, float alpha, float& l_reg, bf16x8& pa0, bf16x8& pa1, bf16x8& pa2, bf16x8& pa3) {
;     for (int r = 0; r < 16; ++r) p1[r] = __builtin_amdgcn_exp2f(p1[r]);
;     float ps = 0; for (int r = 0; r < 16; ++r) ps += p0[r]; for (int r = 0; r < 16; ++r) ps += p1[r];
;     { auto rr = __builtin_amdgcn_permlane32_swap(__float_as_uint(ps), __float_as_uint(ps), false, false);
;       ps = __uint_as_float(rr[0]) + __uint_as_float(rr[1]); }
;     l_reg = l_reg * alpha + ps;
;     ...
;     PK4(p0, 0, pa0); PK4(p0, 8, pa1); PK4(p1, 0, pa2); PK4(p1, 8, pa3);
;     ...
; }
; template <int KB, bool SK, bool BIAS>
; __device__ __forceinline__ void qkt(f32x16& p0, f32x16& p1, const char* K_lds, int r32, int hi, const bf16x8* qr, bool act, const float* bl) {
;     if (SK && !act) { const float NEG = -__builtin_inff();
; #pragma unroll
;         for (int r = 0; r < 16; ++r) { p0[r] = NEG; p1[r] = NEG; } return; }
;     if constexpr (BIAS) {
; #pragma unroll
;         for (int g_ = 0; g_ < 4; ++g_) { const f32x4 t0 = *(const f32x4*)(bl + 8 * g_), t1 = *(const f32x4*)(bl + 32 + 8 * g_);
;             p0[4 * g_] = t0[0]; p0[4 * g_ + 1] = t0[1]; p0[4 * g_ + 2] = t0[2]; p0[4 * g_ + 3] = t0[3]; p1[4 * g_] = t1[0]; p1[4 * g_ + 1] = t1[1]; p1[4 * g_ + 2] = t1[2]; p1[4 * g_ + 3] = t1[3]; }
;     } else { p0 = f32x16{}; p1 = f32x16{}; }
;     const char* kb[4];
; #pragma unroll
;     for (int dd = 0; dd < 4; ++dd) kb[dd] = K_lds + KB * SHM_K + KSWZ(r32, (dd * 16 + hi * 8) * 2);
; #pragma unroll
;     for (int d0 = 0; d0 < 8; ++d0) { const char* a = kb[d0 & 3] + (d0 >> 2) * 128;
;         bf16x8 b0 = *reinterpret_cast<const bf16x8*>(a);
;         bf16x8 b1 = *reinterpret_cast<const bf16x8*>(a + 32 * 256);
;         p0 = __builtin_amdgcn_mfma_f32_32x32x16_bf16(b0, qr[d0], p0, 0, 0, 0);
;         p1 = __builtin_amdgcn_mfma_f32_32x32x16_bf16(b1, qr[d0], p1, 0, 0, 0); }
.Lattn_k2skip_2:
	ds_read_b128 v[114:117], v221 offset:256
	ds_read_b128 v[118:121], v221 offset:288
	ds_read_b128 v[98:101], v221 offset:384
	ds_read_b128 v[102:105], v221 offset:416
	ds_read_b128 v[122:125], v221 offset:320
	ds_read_b128 v[106:109], v221 offset:448
	ds_read_b128 v[126:129], v221 offset:352
	ds_read_b128 v[110:113], v221 offset:480
	ds_read_b128 v[82:85], v208 offset:32768
	ds_read_b128 v[182:185], v208 offset:40960
	v_exp_f32_e32 v87, v87
	v_exp_f32_e32 v88, v88
	v_exp_f32_e32 v89, v89
	s_waitcnt lgkmcnt(1)
	v_mfma_f32_32x32x16_bf16 v[114:129], v[82:85], v[158:161], v[114:129]
	v_exp_f32_e32 v90, v90
	v_exp_f32_e32 v91, v91
	v_exp_f32_e32 v92, v92
	v_exp_f32_e32 v93, v93
	v_exp_f32_e32 v94, v94
	s_waitcnt lgkmcnt(0)
	v_mfma_f32_32x32x16_bf16 v[98:113], v[182:185], v[158:161], v[98:113]
	ds_read_b128 v[82:85], v209 offset:32768
	ds_read_b128 v[182:185], v209 offset:40960
	s_waitcnt lgkmcnt(1)
	v_mfma_f32_32x32x16_bf16 v[114:129], v[82:85], v[154:157], v[114:129]
	s_waitcnt lgkmcnt(0)
	v_mfma_f32_32x32x16_bf16 v[98:113], v[182:185], v[154:157], v[98:113]
	ds_read_b128 v[82:85], v211 offset:32768
	ds_read_b128 v[182:185], v211 offset:40960
	s_waitcnt lgkmcnt(1)
	v_mfma_f32_32x32x16_bf16 v[114:129], v[82:85], v[150:153], v[114:129]
	s_waitcnt lgkmcnt(0)
	v_mfma_f32_32x32x16_bf16 v[98:113], v[182:185], v[150:153], v[98:113]
	ds_read_b128 v[82:85], v212 offset:32768
	ds_read_b128 v[182:185], v212 offset:40960
	s_waitcnt lgkmcnt(1)
	v_mfma_f32_32x32x16_bf16 v[114:129], v[82:85], v[146:149], v[114:129]
	s_waitcnt lgkmcnt(0)
	v_mfma_f32_32x32x16_bf16 v[98:113], v[182:185], v[146:149], v[98:113]
	ds_read_b128 v[82:85], v208 offset:32896
	ds_read_b128 v[182:185], v208 offset:41088
	s_waitcnt lgkmcnt(1)
	v_mfma_f32_32x32x16_bf16 v[114:129], v[82:85], v[142:145], v[114:129]
	s_waitcnt lgkmcnt(0)
	v_mfma_f32_32x32x16_bf16 v[98:113], v[182:185], v[142:145], v[98:113]
	ds_read_b128 v[82:85], v209 offset:32896
	ds_read_b128 v[182:185], v209 offset:41088
	s_waitcnt lgkmcnt(1)
	v_mfma_f32_32x32x16_bf16 v[114:129], v[82:85], v[138:141], v[114:129]
	s_waitcnt lgkmcnt(0)
	v_mfma_f32_32x32x16_bf16 v[98:113], v[182:185], v[138:141], v[98:113]
	ds_read_b128 v[82:85], v211 offset:32896
	ds_read_b128 v[182:185], v211 offset:41088
	s_waitcnt lgkmcnt(1)
	v_mfma_f32_32x32x16_bf16 v[114:129], v[82:85], v[134:137], v[114:129]
	s_waitcnt lgkmcnt(0)
	v_mfma_f32_32x32x16_bf16 v[98:113], v[182:185], v[134:137], v[98:113]
	ds_read_b128 v[82:85], v212 offset:32896
	ds_read_b128 v[182:185], v212 offset:41088
	s_waitcnt lgkmcnt(1)
	v_mfma_f32_32x32x16_bf16 v[114:129], v[82:85], v[130:133], v[114:129]
	v_exp_f32_e32 v85, v97
	v_exp_f32_e32 v97, v178
	v_add_f32_e32 v178, 0, v66
	v_add_f32_e32 v178, v67, v178
	v_add_f32_e32 v178, v68, v178
	v_add_f32_e32 v178, v69, v178
	v_add_f32_e32 v178, v70, v178
	v_add_f32_e32 v178, v71, v178
	v_add_f32_e32 v178, v72, v178
	v_add_f32_e32 v178, v73, v178
	v_add_f32_e32 v178, v74, v178
	v_add_f32_e32 v178, v75, v178
	v_add_f32_e32 v178, v76, v178
	v_add_f32_e32 v178, v77, v178
	v_exp_f32_e32 v82, v86
	v_add_f32_e32 v178, v78, v178
	v_exp_f32_e32 v83, v95
	v_add_f32_e32 v178, v79, v178
	v_exp_f32_e32 v84, v96
	v_add_f32_e32 v178, v80, v178
	v_add_f32_e32 v178, v81, v178
	v_exp_f32_e32 v86, v179
	v_add_f32_e32 v178, v82, v178
	v_add_f32_e32 v178, v83, v178
	v_add_f32_e32 v178, v84, v178
	v_add_f32_e32 v178, v85, v178
	v_add_f32_e32 v178, v86, v178
	v_add_f32_e32 v178, v87, v178
	v_add_f32_e32 v178, v88, v178
	v_add_f32_e32 v178, v89, v178
	v_add_f32_e32 v178, v90, v178
	v_exp_f32_e32 v95, v180
	v_add_f32_e32 v178, v91, v178
	s_waitcnt lgkmcnt(0)
	v_mfma_f32_32x32x16_bf16 v[98:113], v[182:185], v[130:133], v[98:113]
	v_exp_f32_e32 v96, v181
	v_add_f32_e32 v178, v92, v178
	v_add_f32_e32 v178, v93, v178
	v_add_f32_e32 v178, v94, v178
	v_add_f32_e32 v178, v95, v178
	v_add_f32_e32 v178, v96, v178
	v_add_f32_e32 v227, v97, v178
	v_mov_b32_e32 v228, v227
	v_cvt_pk_bf16_f32 v178, v66, v67
	v_cvt_pk_bf16_f32 v179, v68, v69
	v_cvt_pk_bf16_f32 v180, v70, v71
	v_cvt_pk_bf16_f32 v181, v72, v73
	v_cvt_pk_bf16_f32 v182, v74, v75
	v_cvt_pk_bf16_f32 v183, v76, v77
	v_cvt_pk_bf16_f32 v184, v78, v79
	v_cvt_pk_bf16_f32 v185, v80, v81
	v_cvt_pk_bf16_f32 v186, v82, v83
	v_cvt_pk_bf16_f32 v187, v84, v85
	v_cvt_pk_bf16_f32 v188, v86, v87
	v_cvt_pk_bf16_f32 v189, v88, v89
	v_cvt_pk_bf16_f32 v190, v90, v91
	v_cvt_pk_bf16_f32 v191, v92, v93
	v_cvt_pk_bf16_f32 v192, v94, v95
	v_cvt_pk_bf16_f32 v193, v96, v97
	s_nop 1
	v_permlane32_swap_b32_e32 v227, v228
	v_permlane32_swap_b32_e32 v178, v180
	v_permlane32_swap_b32_e32 v179, v181
	v_permlane32_swap_b32_e32 v182, v184
	v_permlane32_swap_b32_e32 v183, v185
	v_permlane32_swap_b32_e32 v186, v188
	v_permlane32_swap_b32_e32 v187, v189
	v_permlane32_swap_b32_e32 v190, v192
	v_permlane32_swap_b32_e32 v191, v193
	s_add_i32 s6, s17, 1
	s_cmp_lt_i32 s6, s31
	s_cselect_b64 s[18:19], -1, 0
	s_cmp_ge_i32 s6, s31
	s_cbranch_scc1 .LBB0_651

; __device__ __forceinline__ void partialSM(f32x16& p0, f32x16& p1, float& m_reg, float& mn, float& alpha) {
;     float pmax = p0[0]; for (int r = 1; r < 16; ++r) pmax = fmaxf(pmax, p0[r]); for (int r = 0; r < 16; ++r) pmax = fmaxf(pmax, p1[r]);
;     { auto rr = __builtin_amdgcn_permlane32_swap(__float_as_uint(pmax), __float_as_uint(pmax), false, false);
;       pmax = fmaxf(__uint_as_float(rr[0]), __uint_as_float(rr[1])); }
;     constexpr float C2 = 1.4426950408889634f * SCALE;
;     if (__builtin_expect(__all((pmax - m_reg) * SCALE <= THR), 1)) { mn = m_reg; alpha = 1.f; }
.LBB0_653:
	v_max_f32_e32 v178, v115, v115
	v_max_f32_e32 v179, v114, v114
	v_max_f32_e32 v178, v179, v178
	v_max3_f32 v178, v178, v116, v117
	v_max3_f32 v178, v178, v118, v119
	v_max3_f32 v178, v178, v120, v121
	v_max3_f32 v178, v178, v122, v123
	v_max3_f32 v178, v178, v124, v125
	v_max3_f32 v178, v178, v126, v127
	v_max3_f32 v178, v178, v128, v129
	v_max3_f32 v178, v178, v98, v99
	v_max3_f32 v178, v178, v100, v101
	v_max3_f32 v178, v178, v102, v103
	v_max3_f32 v178, v178, v104, v105
	v_max3_f32 v178, v178, v106, v107
	v_max3_f32 v178, v178, v108, v109
	v_max3_f32 v178, v178, v110, v111
	v_max3_f32 v178, v178, v112, v113
	v_mov_b32_e32 v179, v178
	s_nop 1
	v_permlane32_swap_b32_e32 v178, v179
	v_max_f32_e32 v179, v179, v179
	v_max_f32_e32 v178, v178, v178
	v_max_f32_e32 v178, v178, v179
	v_sub_f32_e32 v179, v178, v226
	v_mul_f32_e32 v179, 0x3db504f3, v179
	v_cmp_ge_f32_e32 vcc, s26, v179
	s_cmp_eq_u64 vcc, exec
	s_cselect_b64 s[6:7], -1, 0
	s_andn2_b64 vcc, exec, s[18:19]
	s_barrier
	s_cbranch_vccnz .Lattn_vskip_2
	s_add_u32 s98, s0, 0x9660000
	s_addc_u32 s99, s1, 0
	s_lshl_b32 s100, s75, 10
	s_add_i32 m0, s100, 0x4000
	s_nop 0
	global_load_lds_dwordx4 v254, s[98:99]
	s_add_u32 s98, s98, 0x10000
	s_addc_u32 s99, s99, 0
	s_add_i32 m0, m0, 0x2000
	s_nop 0
	global_load_lds_dwordx4 v254, s[98:99]
	s_waitcnt vmcnt(2)
	s_branch .LBB0_655

; __device__ __forceinline__ void partialSM(f32x16& p0, f32x16& p1, float& m_reg, float& mn, float& alpha) {
;     ...
;     constexpr float C2 = 1.4426950408889634f * SCALE;
;     if (__builtin_expect(__all((pmax - m_reg) * SCALE <= THR), 1)) { mn = m_reg; alpha = 1.f; }
;     else { mn = fmaxf(m_reg, pmax); alpha = __builtin_amdgcn_exp2f((m_reg - mn) * C2); m_reg = mn; }
.LBB0_655:
	v_max_f32_e32 v162, v226, v226
	v_max_f32_e32 v162, v162, v178
	v_sub_f32_e32 v163, v226, v162
	v_mul_f32_e32 v163, 0x3e0293ee, v163
	v_exp_f32_e32 v163, v163
	v_cndmask_b32_e64 v166, v163, 1.0, s[6:7]
	v_cmp_gt_f32_e32 vcc, 1.0, v166
	s_cbranch_vccz .LBB0_642
	s_and_saveexec_b64 s[18:19], s[4:5]
	s_cbranch_execz .LBB0_641
	ds_write_b32 v218, v166 offset:128
	s_branch .LBB0_641

; #define SBAR() __builtin_amdgcn_sched_barrier(0)
; #define BL(t) (bias0 + KBASE(t))
; #define ACT(t) (KBASE(t) <= qlo + QBLK - 1 && KBASE(t) + KVBLK - 1 >= qlo - W + 1)
; template <int KB, bool SK, bool BIAS>
; __device__ __forceinline__ void qkt(f32x16& p0, f32x16& p1, const char* K_lds, int r32, int hi, const bf16x8* qr, bool act, const float* bl) {
;     if (SK && !act) { const float NEG = -__builtin_inff();
; #pragma unroll
;         for (int r = 0; r < 16; ++r) { p0[r] = NEG; p1[r] = NEG; } return; }
;     if constexpr (BIAS) {
; #pragma unroll
;         for (int g_ = 0; g_ < 4; ++g_) { const f32x4 t0 = *(const f32x4*)(bl + 8 * g_), t1 = *(const f32x4*)(bl + 32 + 8 * g_);
;             p0[4 * g_] = t0[0]; p0[4 * g_ + 1] = t0[1]; p0[4 * g_ + 2] = t0[2]; p0[4 * g_ + 3] = t0[3]; p1[4 * g_] = t1[0]; p1[4 * g_ + 1] = t1[1]; p1[4 * g_ + 2] = t1[2]; p1[4 * g_ + 3] = t1[3]; }
;     } else { p0 = f32x16{}; p1 = f32x16{}; }
;     const char* kb[4];
; #pragma unroll
;     for (int dd = 0; dd < 4; ++dd) kb[dd] = K_lds + KB * SHM_K + KSWZ(r32, (dd * 16 + hi * 8) * 2);
; #pragma unroll
;     for (int d0 = 0; d0 < 8; ++d0) { const char* a = kb[d0 & 3] + (d0 >> 2) * 128;
;         bf16x8 b0 = *reinterpret_cast<const bf16x8*>(a);
;         bf16x8 b1 = *reinterpret_cast<const bf16x8*>(a + 32 * 256);
;         p0 = __builtin_amdgcn_mfma_f32_32x32x16_bf16(b0, qr[d0], p0, 0, 0, 0);
;         p1 = __builtin_amdgcn_mfma_f32_32x32x16_bf16(b1, qr[d0], p1, 0, 0, 0); }
; template <class TIn, class TOut, int QS, int KS, int OS, bool BIAS, bool PREF = true>
; __device__ __forceinline__ void causal_swa_block(const BlockRef<TIn, TOut>& cur, const BlockRef<TIn, TOut>& nxt, int skv, int W, char* lds, Seam<TIn>& S) {
;     ...
;     const bool even = (NT & 1) == 0;
;     if (even) { SBAR(); qkt<1, SK, BIAS>(pB0, pB1, K_lds, r32, hi, S.qr, ACT(NT - 1), BL(NT - 1)); SBAR(); }
.LBB0_659:
	s_waitcnt vmcnt(0)
	s_bitcmp0_b32 s31, 0
	s_cselect_b64 s[0:1], -1, 0
	s_and_b64 vcc, exec, s[0:1]
	s_cbranch_vccz .LBB0_661
	v_lshl_add_u32 v94, s15, 8, v210
	v_add_u32_e32 v66, 0xffffff00, v94
	v_add_u32_e32 v70, 0xffffff80, v94
	ds_read_b128 v[66:69], v66
	ds_read_b128 v[82:85], v70
	v_add_u32_e32 v70, 0xffffff20, v94
	v_add_u32_e32 v74, 0xffffffa0, v94
	ds_read_b128 v[70:73], v70
	ds_read_b128 v[86:89], v74
	ds_read_b128 v[98:101], v208 offset:49152
	v_add_u32_e32 v74, 0xffffff40, v94
	v_subrev_u32_e32 v90, 64, v94
	v_add_u32_e32 v75, 0xffffff60, v94
	ds_read_b128 v[78:81], v75
	ds_read_b128 v[74:77], v74
	ds_read_b128 v[90:93], v90
	v_subrev_u32_e32 v94, 32, v94
	ds_read_b128 v[94:97], v94
	ds_read_b128 v[166:169], v208 offset:49280
	s_waitcnt lgkmcnt(3)
	v_mfma_f32_32x32x16_bf16 v[66:81], v[98:101], v[158:161], v[66:81]
	ds_read_b128 v[98:101], v208 offset:57344
	ds_read_b128 v[170:173], v208 offset:57472
	s_waitcnt lgkmcnt(1)
	v_mfma_f32_32x32x16_bf16 v[82:97], v[98:101], v[158:161], v[82:97]
	ds_read_b128 v[98:101], v209 offset:49152
	ds_read_b128 v[158:161], v209 offset:49280
	s_waitcnt lgkmcnt(1)
	v_mfma_f32_32x32x16_bf16 v[66:81], v[98:101], v[154:157], v[66:81]
	ds_read_b128 v[98:101], v209 offset:57344
	s_waitcnt vmcnt(0)
	ds_read_b128 v[174:177], v209 offset:57472
	s_waitcnt lgkmcnt(1)
	v_mfma_f32_32x32x16_bf16 v[82:97], v[98:101], v[154:157], v[82:97]
	ds_read_b128 v[98:101], v211 offset:49152
	ds_read_b128 v[154:157], v211 offset:49280
	s_waitcnt lgkmcnt(1)
	v_mfma_f32_32x32x16_bf16 v[66:81], v[98:101], v[150:153], v[66:81]
	ds_read_b128 v[98:101], v211 offset:57344
	ds_read_b128 v[180:183], v211 offset:57472
	s_waitcnt lgkmcnt(1)
	v_mfma_f32_32x32x16_bf16 v[82:97], v[98:101], v[150:153], v[82:97]
	ds_read_b128 v[98:101], v212 offset:49152
	ds_read_b128 v[150:153], v212 offset:49280
	s_waitcnt lgkmcnt(1)
	v_mfma_f32_32x32x16_bf16 v[66:81], v[98:101], v[146:149], v[66:81]
	ds_read_b128 v[98:101], v212 offset:57344
	ds_read_b128 v[184:187], v212 offset:57472
	s_waitcnt lgkmcnt(1)
	v_mfma_f32_32x32x16_bf16 v[82:97], v[98:101], v[146:149], v[82:97]
	v_mfma_f32_32x32x16_bf16 v[66:81], v[166:169], v[142:145], v[66:81]
	v_mfma_f32_32x32x16_bf16 v[82:97], v[170:173], v[142:145], v[82:97]
	v_mfma_f32_32x32x16_bf16 v[66:81], v[158:161], v[138:141], v[66:81]
	v_mfma_f32_32x32x16_bf16 v[82:97], v[174:177], v[138:141], v[82:97]
	v_mfma_f32_32x32x16_bf16 v[66:81], v[154:157], v[134:137], v[66:81]
	v_mfma_f32_32x32x16_bf16 v[82:97], v[180:183], v[134:137], v[82:97]
	v_mfma_f32_32x32x16_bf16 v[66:81], v[150:153], v[130:133], v[66:81]
	s_waitcnt lgkmcnt(0)
	v_mfma_f32_32x32x16_bf16 v[82:97], v[184:187], v[130:133], v[82:97]

; __global__ void __launch_bounds__(NTHREADS, 2) mega_fwd(KArgs args) {
;     extern __shared__ __attribute__((aligned(16))) unsigned char lds_raw[];
	.amdhsa_kernel _Z8mega_fwd5KArgs
		.amdhsa_group_segment_fixed_size 0
		.amdhsa_private_segment_fixed_size 0
		.amdhsa_kernarg_size 488
		.amdhsa_user_sgpr_count 2
		.amdhsa_user_sgpr_dispatch_ptr 0
		.amdhsa_user_sgpr_queue_ptr 0
		.amdhsa_user_sgpr_kernarg_segment_ptr 1
		.amdhsa_user_sgpr_dispatch_id 0
		.amdhsa_user_sgpr_kernarg_preload_length 0
		.amdhsa_user_sgpr_kernarg_preload_offset 0
		.amdhsa_user_sgpr_private_segment_size 0
		.amdhsa_uses_dynamic_stack 0
		.amdhsa_enable_private_segment 0
		.amdhsa_system_sgpr_workgroup_id_x 1
		.amdhsa_system_sgpr_workgroup_id_y 0
		.amdhsa_system_sgpr_workgroup_id_z 0
		.amdhsa_system_sgpr_workgroup_info 0
		.amdhsa_system_vgpr_workitem_id 0
		.amdhsa_next_free_vgpr 256
		.amdhsa_next_free_sgpr 102
		.amdhsa_accum_offset 256
		.amdhsa_reserve_vcc 1
		.amdhsa_float_round_mode_32 0
		.amdhsa_float_round_mode_16_64 0
		.amdhsa_float_denorm_mode_32 3
		.amdhsa_float_denorm_mode_16_64 3
		.amdhsa_dx10_clamp 1
		.amdhsa_ieee_mode 1
		.amdhsa_fp16_overflow 0
		.amdhsa_tg_split 0
		.amdhsa_exception_fp_ieee_invalid_op 0
		.amdhsa_exception_fp_denorm_src 0
		.amdhsa_exception_fp_ieee_div_zero 0
		.amdhsa_exception_fp_ieee_overflow 0
		.amdhsa_exception_fp_ieee_underflow 0
		.amdhsa_exception_fp_ieee_inexact 0
		.amdhsa_exception_int_div_zero 0
	.end_amdhsa_kernel

; __global__ void __launch_bounds__(NTHREADS, 2) mega_fwd(KArgs args) {
;     extern __shared__ __attribute__((aligned(16))) unsigned char lds_raw[];
amdhsa.kernels:
  - .agpr_count:     0
    .args:
      - .offset:         0
        .size:           232
        .value_kind:     by_value
      - .offset:         232
        .size:           4
        .value_kind:     hidden_block_count_x
      - .offset:         236
        .size:           4
        .value_kind:     hidden_block_count_y
      - .offset:         240
        .size:           4
        .value_kind:     hidden_block_count_z
      - .offset:         244
        .size:           2
        .value_kind:     hidden_group_size_x
      - .offset:         246
        .size:           2
        .value_kind:     hidden_group_size_y
      - .offset:         248
        .size:           2
        .value_kind:     hidden_group_size_z
      - .offset:         250
        .size:           2
        .value_kind:     hidden_remainder_x
      - .offset:         252
        .size:           2
        .value_kind:     hidden_remainder_y
      - .offset:         254
        .size:           2
        .value_kind:     hidden_remainder_z
      - .offset:         272
        .size:           8
        .value_kind:     hidden_global_offset_x
      - .offset:         280
        .size:           8
        .value_kind:     hidden_global_offset_y
      - .offset:         288
        .size:           8
        .value_kind:     hidden_global_offset_z
      - .offset:         296
        .size:           2
        .value_kind:     hidden_grid_dims
      - .offset:         352
        .size:           4
        .value_kind:     hidden_dynamic_lds_size
    .group_segment_fixed_size: 0
    .kernarg_segment_align: 8
    .kernarg_segment_size: 488
    .language:       OpenCL C
    .language_version:
      - 2
      - 0
    .max_flat_workgroup_size: 512
    .name:           _Z8mega_fwd5KArgs
    .private_segment_fixed_size: 0
    .sgpr_count:     108
    .sgpr_spill_count: 336
    .symbol:         _Z8mega_fwd5KArgs.kd
    .uniform_work_group_size: 1
    .uses_dynamic_stack: false
    .vgpr_count:     256
    .vgpr_spill_count: 0
    .wavefront_size: 64
